# v7: per-cluster s_setprio flips removed from the re-cut (16-MFMA-per-segment) fp8 K-loops
# speedup vs baseline: 1.0060x; 1.0060x over previous
.LBB0_215:
	ds_read_b128 v[10:13], v175
	ds_read_b128 v[14:17], v175 offset:1024
	ds_read_b128 v[166:169], v175 offset:2048
	ds_read_b128 v[170:173], v175 offset:3072
	s_add_u32 s28, s8, 0xfffc0080
	s_addc_u32 s29, s9, -1
	s_cmp_eq_u32 s64, 12
	s_cselect_b32 s31, s13, s29
	s_cselect_b32 s30, s21, s28
	s_cselect_b32 s29, s15, s63
	s_cselect_b32 s28, s51, s62
	s_mov_b32 m0, s52
	v_lshl_add_u64 v[2:3], s[8:9], 0, v[158:159]
	ds_read_b128 v[180:183], v176
	ds_read_b128 v[184:187], v176 offset:1024
	ds_read_b128 v[188:191], v176 offset:2048
	ds_read_b128 v[192:195], v176 offset:3072
	ds_read_b128 v[196:199], v176 offset:4096
	ds_read_b128 v[200:203], v176 offset:5120
	ds_read_b128 v[204:207], v176 offset:6144
	ds_read_b128 v[208:211], v176 offset:7168
	global_load_lds_dwordx4 v[2:3], off
	v_lshl_add_u64 v[2:3], s[8:9], 0, v[160:161]
	s_mov_b32 m0, s53
	s_nop 0
	global_load_lds_dwordx4 v[2:3], off
	ds_read_b128 v[212:215], v177
	ds_read_b128 v[216:219], v177 offset:1024
	ds_read_b128 v[220:223], v177 offset:2048
	ds_read_b128 v[224:227], v177 offset:3072
	s_waitcnt vmcnt(8) lgkmcnt(0)
	s_barrier
	v_mfma_f32_16x16x128_f8f6f4 v[138:141], v[10:17], v[180:187], v[138:141]
	v_mfma_f32_16x16x128_f8f6f4 v[134:137], v[166:173], v[180:187], v[134:137]
	v_mfma_f32_16x16x128_f8f6f4 v[122:125], v[10:17], v[188:195], v[122:125]
	v_mfma_f32_16x16x128_f8f6f4 v[118:121], v[166:173], v[188:195], v[118:121]
	v_mfma_f32_16x16x128_f8f6f4 v[98:101], v[10:17], v[196:203], v[98:101]
	v_mfma_f32_16x16x128_f8f6f4 v[90:93], v[166:173], v[196:203], v[90:93]
	v_mfma_f32_16x16x128_f8f6f4 v[70:73], v[10:17], v[204:211], v[70:73]
	v_mfma_f32_16x16x128_f8f6f4 v[58:61], v[166:173], v[204:211], v[58:61]
	v_mfma_f32_16x16x128_f8f6f4 v[146:149], v[212:219], v[180:187], v[146:149]
	v_mfma_f32_16x16x128_f8f6f4 v[142:145], v[220:227], v[180:187], v[142:145]
	v_mfma_f32_16x16x128_f8f6f4 v[130:133], v[212:219], v[188:195], v[130:133]
	v_mfma_f32_16x16x128_f8f6f4 v[126:129], v[220:227], v[188:195], v[126:129]
	v_mfma_f32_16x16x128_f8f6f4 v[114:117], v[212:219], v[196:203], v[114:117]
	v_mfma_f32_16x16x128_f8f6f4 v[110:113], v[220:227], v[196:203], v[110:113]
	v_mfma_f32_16x16x128_f8f6f4 v[82:85], v[212:219], v[204:211], v[82:85]
	v_mfma_f32_16x16x128_f8f6f4 v[78:81], v[220:227], v[204:211], v[78:81]
	s_barrier
	ds_read_b128 v[180:183], v176 offset:16384
	ds_read_b128 v[184:187], v176 offset:17408
	ds_read_b128 v[188:191], v176 offset:18432
	ds_read_b128 v[192:195], v176 offset:19456
	ds_read_b128 v[196:199], v176 offset:20480
	ds_read_b128 v[200:203], v176 offset:21504
	ds_read_b128 v[204:207], v176 offset:22528
	ds_read_b128 v[208:211], v176 offset:23552
	s_mov_b32 m0, s54
	v_lshl_add_u64 v[6:7], s[28:29], 0, v[154:155]
	global_load_lds_dwordx4 v[6:7], off
	v_lshl_add_u64 v[8:9], s[28:29], 0, v[150:151]
	s_mov_b32 m0, s55
	s_nop 0
	global_load_lds_dwordx4 v[8:9], off
	s_mov_b32 m0, s27
	v_lshl_add_u64 v[2:3], s[30:31], 0, v[156:157]
	global_load_lds_dwordx4 v[2:3], off
	v_lshl_add_u64 v[4:5], s[30:31], 0, v[152:153]
	s_mov_b32 m0, s41
	s_nop 0
	global_load_lds_dwordx4 v[4:5], off
	s_add_u32 s66, s28, 0x40000
	s_addc_u32 s67, s29, 0
	s_mov_b32 m0, s56
	v_lshl_add_u64 v[228:229], s[66:67], 0, v[154:155]
	global_load_lds_dwordx4 v[228:229], off
	v_lshl_add_u64 v[228:229], s[66:67], 0, v[150:151]
	s_mov_b32 m0, s57
	s_nop 0
	global_load_lds_dwordx4 v[228:229], off
	s_waitcnt vmcnt(8) lgkmcnt(0)
	s_barrier
	v_mfma_f32_16x16x128_f8f6f4 v[94:97], v[10:17], v[180:187], v[94:97]
	v_mfma_f32_16x16x128_f8f6f4 v[86:89], v[166:173], v[180:187], v[86:89]
	v_mfma_f32_16x16x128_f8f6f4 v[66:69], v[10:17], v[188:195], v[66:69]
	v_mfma_f32_16x16x128_f8f6f4 v[54:57], v[166:173], v[188:195], v[54:57]
	v_mfma_f32_16x16x128_f8f6f4 v[46:49], v[10:17], v[196:203], v[46:49]
	v_mfma_f32_16x16x128_f8f6f4 v[38:41], v[166:173], v[196:203], v[38:41]
	v_mfma_f32_16x16x128_f8f6f4 v[30:33], v[10:17], v[204:211], v[30:33]
	v_mfma_f32_16x16x128_f8f6f4 v[22:25], v[166:173], v[204:211], v[22:25]
	v_mfma_f32_16x16x128_f8f6f4 v[106:109], v[212:219], v[180:187], v[106:109]
	v_mfma_f32_16x16x128_f8f6f4 v[102:105], v[220:227], v[180:187], v[102:105]
	v_mfma_f32_16x16x128_f8f6f4 v[74:77], v[212:219], v[188:195], v[74:77]
	v_mfma_f32_16x16x128_f8f6f4 v[62:65], v[220:227], v[188:195], v[62:65]
	v_mfma_f32_16x16x128_f8f6f4 v[50:53], v[212:219], v[196:203], v[50:53]
	v_mfma_f32_16x16x128_f8f6f4 v[42:45], v[220:227], v[196:203], v[42:45]
	v_mfma_f32_16x16x128_f8f6f4 v[34:37], v[212:219], v[204:211], v[34:37]
	v_mfma_f32_16x16x128_f8f6f4 v[26:29], v[220:227], v[204:211], v[26:29]
	s_barrier
	ds_read_b128 v[10:13], v178
	ds_read_b128 v[14:17], v178 offset:1024
	ds_read_b128 v[166:169], v178 offset:2048
	ds_read_b128 v[170:173], v178 offset:3072
	s_add_u32 s30, s30, 0x40000
	s_addc_u32 s31, s31, 0
	s_mov_b32 m0, s42
	v_lshl_add_u64 v[212:213], s[30:31], 0, v[156:157]
	ds_read_b128 v[180:183], v176 offset:32768
	ds_read_b128 v[184:187], v176 offset:33792
	ds_read_b128 v[188:191], v176 offset:34816
	ds_read_b128 v[192:195], v176 offset:35840
	ds_read_b128 v[196:199], v176 offset:36864
	ds_read_b128 v[200:203], v176 offset:37888
	ds_read_b128 v[204:207], v176 offset:38912
	ds_read_b128 v[208:211], v176 offset:39936
	global_load_lds_dwordx4 v[212:213], off
	v_lshl_add_u64 v[212:213], s[30:31], 0, v[152:153]
	s_mov_b32 m0, s43
	s_nop 0
	global_load_lds_dwordx4 v[212:213], off
	ds_read_b128 v[212:215], v179
	ds_read_b128 v[216:219], v179 offset:1024
	ds_read_b128 v[220:223], v179 offset:2048
	ds_read_b128 v[224:227], v179 offset:3072
	s_waitcnt vmcnt(8) lgkmcnt(0)
	s_barrier
	v_mfma_f32_16x16x128_f8f6f4 v[138:141], v[10:17], v[180:187], v[138:141]
	v_mfma_f32_16x16x128_f8f6f4 v[134:137], v[166:173], v[180:187], v[134:137]
	v_mfma_f32_16x16x128_f8f6f4 v[122:125], v[10:17], v[188:195], v[122:125]
	v_mfma_f32_16x16x128_f8f6f4 v[118:121], v[166:173], v[188:195], v[118:121]
	v_mfma_f32_16x16x128_f8f6f4 v[98:101], v[10:17], v[196:203], v[98:101]
	v_mfma_f32_16x16x128_f8f6f4 v[90:93], v[166:173], v[196:203], v[90:93]
	v_mfma_f32_16x16x128_f8f6f4 v[70:73], v[10:17], v[204:211], v[70:73]
	v_mfma_f32_16x16x128_f8f6f4 v[58:61], v[166:173], v[204:211], v[58:61]
	v_mfma_f32_16x16x128_f8f6f4 v[146:149], v[212:219], v[180:187], v[146:149]
	v_mfma_f32_16x16x128_f8f6f4 v[142:145], v[220:227], v[180:187], v[142:145]
	v_mfma_f32_16x16x128_f8f6f4 v[130:133], v[212:219], v[188:195], v[130:133]
	v_mfma_f32_16x16x128_f8f6f4 v[126:129], v[220:227], v[188:195], v[126:129]
	v_mfma_f32_16x16x128_f8f6f4 v[114:117], v[212:219], v[196:203], v[114:117]
	v_mfma_f32_16x16x128_f8f6f4 v[110:113], v[220:227], v[196:203], v[110:113]
	v_mfma_f32_16x16x128_f8f6f4 v[82:85], v[212:219], v[204:211], v[82:85]
	v_mfma_f32_16x16x128_f8f6f4 v[78:81], v[220:227], v[204:211], v[78:81]
	s_barrier
	ds_read_b128 v[180:183], v176 offset:49152
	ds_read_b128 v[184:187], v176 offset:50176
	ds_read_b128 v[188:191], v176 offset:51200
	ds_read_b128 v[192:195], v176 offset:52224
	ds_read_b128 v[196:199], v176 offset:53248
	ds_read_b128 v[200:203], v176 offset:54272
	ds_read_b128 v[204:207], v176 offset:55296
	ds_read_b128 v[208:211], v176 offset:56320
	s_mov_b32 m0, s58
	v_lshl_add_u64 v[6:7], v[6:7], 0, s[4:5]
	global_load_lds_dwordx4 v[6:7], off
	v_lshl_add_u64 v[6:7], v[8:9], 0, s[4:5]
	s_mov_b32 m0, s59
	s_nop 0
	global_load_lds_dwordx4 v[6:7], off
	s_mov_b32 m0, s44
	v_lshl_add_u64 v[2:3], v[2:3], 0, s[4:5]
	global_load_lds_dwordx4 v[2:3], off
	v_lshl_add_u64 v[2:3], v[4:5], 0, s[4:5]
	s_mov_b32 m0, s45
	s_nop 0
	global_load_lds_dwordx4 v[2:3], off
	s_add_u32 s28, s28, 0x40080
	s_addc_u32 s29, s29, 0
	s_mov_b32 m0, s60
	v_lshl_add_u64 v[2:3], s[28:29], 0, v[154:155]
	global_load_lds_dwordx4 v[2:3], off
	v_lshl_add_u64 v[2:3], s[28:29], 0, v[150:151]
	s_mov_b32 m0, s61
	s_nop 0
	global_load_lds_dwordx4 v[2:3], off
	s_waitcnt vmcnt(8) lgkmcnt(0)
	s_barrier
	v_mfma_f32_16x16x128_f8f6f4 v[94:97], v[10:17], v[180:187], v[94:97]
	v_mfma_f32_16x16x128_f8f6f4 v[86:89], v[166:173], v[180:187], v[86:89]
	v_mfma_f32_16x16x128_f8f6f4 v[66:69], v[10:17], v[188:195], v[66:69]
	v_mfma_f32_16x16x128_f8f6f4 v[54:57], v[166:173], v[188:195], v[54:57]
	v_mfma_f32_16x16x128_f8f6f4 v[46:49], v[10:17], v[196:203], v[46:49]
	v_mfma_f32_16x16x128_f8f6f4 v[38:41], v[166:173], v[196:203], v[38:41]
	v_mfma_f32_16x16x128_f8f6f4 v[30:33], v[10:17], v[204:211], v[30:33]
	v_mfma_f32_16x16x128_f8f6f4 v[22:25], v[166:173], v[204:211], v[22:25]
	v_mfma_f32_16x16x128_f8f6f4 v[106:109], v[212:219], v[180:187], v[106:109]
	v_mfma_f32_16x16x128_f8f6f4 v[102:105], v[220:227], v[180:187], v[102:105]
	v_mfma_f32_16x16x128_f8f6f4 v[74:77], v[212:219], v[188:195], v[74:77]
	v_mfma_f32_16x16x128_f8f6f4 v[62:65], v[220:227], v[188:195], v[62:65]
	v_mfma_f32_16x16x128_f8f6f4 v[50:53], v[212:219], v[196:203], v[50:53]
	v_mfma_f32_16x16x128_f8f6f4 v[42:45], v[220:227], v[196:203], v[42:45]
	v_mfma_f32_16x16x128_f8f6f4 v[34:37], v[212:219], v[204:211], v[34:37]
	v_mfma_f32_16x16x128_f8f6f4 v[26:29], v[220:227], v[204:211], v[26:29]
	s_add_i32 s64, s64, 2
	s_add_u32 s8, s8, 0x100
	s_addc_u32 s9, s9, 0
	s_add_u32 s62, s62, 0x100
	s_addc_u32 s63, s63, 0
	s_cmp_gt_u32 s64, 13
	s_barrier
	s_cbranch_scc0 .LBB0_215
	v_mov_b32_e32 v166, v0
	s_nop 15
	s_nop 15
	s_lshl_b32 s9, s26, 8
	v_readfirstlane_b32 s8, v166
	s_ashr_i32 s13, s8, 2
	s_andn2_b32 s13, s13, 63
	s_lshr_b32 s8, s8, 1
	s_add_i32 s13, s13, s9
	s_and_b32 s8, s8, 0x60
	s_lshl_b32 s9, s50, 8
	v_and_or_b32 v178, v166, 15, s13
	v_lshrrev_b32_e32 v166, 1, v166
	s_or_b32 s8, s8, s9
	v_and_or_b32 v168, v166, 24, s8
	v_mov_b64_e32 v[14:15], v[18:19]
	v_mov_b64_e32 v[10:11], v[18:19]
	v_mov_b64_e32 v[6:7], v[18:19]
	v_mov_b64_e32 v[2:3], v[18:19]
	v_ashrrev_i32_e32 v169, 31, v168
	v_mov_b64_e32 v[166:167], s[2:3]
	v_mov_b64_e32 v[16:17], v[20:21]
	v_mov_b64_e32 v[12:13], v[20:21]
	v_mov_b64_e32 v[8:9], v[20:21]
	v_mov_b64_e32 v[4:5], v[20:21]
	v_mad_i64_i32 v[170:171], s[8:9], v178, s49, v[166:167]
	v_lshlrev_b64 v[168:169], 1, v[168:169]
	s_waitcnt vmcnt(6)
	v_lshl_add_u64 v[170:171], v[170:171], 0, v[168:169]
	v_pk_fma_f32 v[140:141], v[140:141], s[18:19], v[16:17] op_sel_hi:[1,0,1]
	v_pk_fma_f32 v[138:139], v[138:139], s[18:19], v[14:15] op_sel_hi:[1,0,1]
	v_pk_fma_f32 v[172:173], v[136:137], s[18:19], v[12:13] op_sel_hi:[1,0,1]
	v_pk_fma_f32 v[136:137], v[134:135], s[18:19], v[10:11] op_sel_hi:[1,0,1]
	v_cvt_pk_bf16_f32 v134, v138, v139
	v_cvt_pk_bf16_f32 v135, v140, v141
	v_pk_fma_f32 v[138:139], v[144:145], s[18:19], v[4:5] op_sel_hi:[1,0,1]
	v_cvt_pk_bf16_f32 v136, v136, v137
	v_cvt_pk_bf16_f32 v137, v172, v173
	global_store_dwordx4 v[170:171], v[134:137], off
	v_pk_fma_f32 v[140:141], v[142:143], s[18:19], v[2:3] op_sel_hi:[1,0,1]
	v_pk_fma_f32 v[124:125], v[124:125], s[18:19], v[16:17] op_sel_hi:[1,0,1]
	v_pk_fma_f32 v[134:135], v[146:147], s[18:19], v[6:7] op_sel_hi:[1,0,1]
	v_pk_fma_f32 v[136:137], v[148:149], s[18:19], v[8:9] op_sel_hi:[1,0,1]
	v_cvt_pk_bf16_f32 v134, v134, v135
	v_pk_fma_f32 v[122:123], v[122:123], s[18:19], v[14:15] op_sel_hi:[1,0,1]
	v_cvt_pk_bf16_f32 v135, v136, v137
	v_cvt_pk_bf16_f32 v136, v140, v141
	v_cvt_pk_bf16_f32 v137, v138, v139
	global_store_dwordx4 v[170:171], v[134:137], off offset:256
	v_pk_fma_f32 v[100:101], v[100:101], s[18:19], v[16:17] op_sel_hi:[1,0,1]
	v_pk_fma_f32 v[98:99], v[98:99], s[18:19], v[14:15] op_sel_hi:[1,0,1]
	v_or_b32_e32 v134, 16, v178
	v_mad_i64_i32 v[134:135], s[8:9], v134, s49, v[166:167]
	v_lshl_add_u64 v[134:135], v[134:135], 0, v[168:169]
	v_pk_fma_f32 v[136:137], v[120:121], s[18:19], v[12:13] op_sel_hi:[1,0,1]
	v_pk_fma_f32 v[120:121], v[118:119], s[18:19], v[10:11] op_sel_hi:[1,0,1]
	v_cvt_pk_bf16_f32 v118, v122, v123
	v_cvt_pk_bf16_f32 v119, v124, v125
	v_pk_fma_f32 v[122:123], v[128:129], s[18:19], v[4:5] op_sel_hi:[1,0,1]
	v_cvt_pk_bf16_f32 v120, v120, v121
	v_cvt_pk_bf16_f32 v121, v136, v137
	global_store_dwordx4 v[134:135], v[118:121], off
	v_pk_fma_f32 v[124:125], v[126:127], s[18:19], v[2:3] op_sel_hi:[1,0,1]
	v_pk_fma_f32 v[72:73], v[72:73], s[18:19], v[16:17] op_sel_hi:[1,0,1]
	v_pk_fma_f32 v[118:119], v[130:131], s[18:19], v[6:7] op_sel_hi:[1,0,1]
	v_pk_fma_f32 v[120:121], v[132:133], s[18:19], v[8:9] op_sel_hi:[1,0,1]
	v_cvt_pk_bf16_f32 v118, v118, v119
	v_pk_fma_f32 v[70:71], v[70:71], s[18:19], v[14:15] op_sel_hi:[1,0,1]
	v_cvt_pk_bf16_f32 v119, v120, v121
	v_cvt_pk_bf16_f32 v120, v124, v125
	v_cvt_pk_bf16_f32 v121, v122, v123
	global_store_dwordx4 v[134:135], v[118:121], off offset:256
	v_pk_fma_f32 v[66:67], v[66:67], s[18:19], v[14:15] op_sel_hi:[1,0,1]
	v_pk_fma_f32 v[62:63], v[62:63], s[18:19], v[2:3] op_sel_hi:[1,0,1]
	v_or_b32_e32 v118, 32, v178
	v_mad_i64_i32 v[118:119], s[8:9], v118, s49, v[166:167]
	v_lshl_add_u64 v[118:119], v[118:119], 0, v[168:169]
	v_pk_fma_f32 v[120:121], v[92:93], s[18:19], v[12:13] op_sel_hi:[1,0,1]
	v_pk_fma_f32 v[92:93], v[90:91], s[18:19], v[10:11] op_sel_hi:[1,0,1]
	v_cvt_pk_bf16_f32 v90, v98, v99
	v_cvt_pk_bf16_f32 v91, v100, v101
	v_pk_fma_f32 v[98:99], v[112:113], s[18:19], v[4:5] op_sel_hi:[1,0,1]
	v_cvt_pk_bf16_f32 v92, v92, v93
	v_cvt_pk_bf16_f32 v93, v120, v121
	global_store_dwordx4 v[118:119], v[90:93], off
	v_pk_fma_f32 v[100:101], v[110:111], s[18:19], v[2:3] op_sel_hi:[1,0,1]
	v_pk_fma_f32 v[48:49], v[48:49], s[18:19], v[16:17] op_sel_hi:[1,0,1]
	v_pk_fma_f32 v[90:91], v[114:115], s[18:19], v[6:7] op_sel_hi:[1,0,1]
	v_pk_fma_f32 v[92:93], v[116:117], s[18:19], v[8:9] op_sel_hi:[1,0,1]
	v_cvt_pk_bf16_f32 v90, v90, v91
	v_pk_fma_f32 v[46:47], v[46:47], s[18:19], v[14:15] op_sel_hi:[1,0,1]
	v_cvt_pk_bf16_f32 v91, v92, v93
	v_cvt_pk_bf16_f32 v92, v100, v101
	v_cvt_pk_bf16_f32 v93, v98, v99
	global_store_dwordx4 v[118:119], v[90:93], off offset:256
	v_pk_fma_f32 v[44:45], v[44:45], s[18:19], v[4:5] op_sel_hi:[1,0,1]
	v_pk_fma_f32 v[42:43], v[42:43], s[18:19], v[2:3] op_sel_hi:[1,0,1]
	v_or_b32_e32 v90, 48, v178
	v_mad_i64_i32 v[90:91], s[8:9], v90, s49, v[166:167]
	v_lshl_add_u64 v[90:91], v[90:91], 0, v[168:169]
	v_pk_fma_f32 v[92:93], v[60:61], s[18:19], v[12:13] op_sel_hi:[1,0,1]
	v_pk_fma_f32 v[60:61], v[58:59], s[18:19], v[10:11] op_sel_hi:[1,0,1]
	v_cvt_pk_bf16_f32 v58, v70, v71
	v_cvt_pk_bf16_f32 v59, v72, v73
	v_pk_fma_f32 v[70:71], v[80:81], s[18:19], v[4:5] op_sel_hi:[1,0,1]
	v_cvt_pk_bf16_f32 v60, v60, v61
	v_cvt_pk_bf16_f32 v61, v92, v93
	global_store_dwordx4 v[90:91], v[58:61], off
	v_pk_fma_f32 v[72:73], v[78:79], s[18:19], v[2:3] op_sel_hi:[1,0,1]
	v_pk_fma_f32 v[78:79], v[86:87], s[18:19], v[10:11] op_sel_hi:[1,0,1]
	v_pk_fma_f32 v[58:59], v[82:83], s[18:19], v[6:7] op_sel_hi:[1,0,1]
	v_pk_fma_f32 v[60:61], v[84:85], s[18:19], v[8:9] op_sel_hi:[1,0,1]
	v_cvt_pk_bf16_f32 v58, v58, v59
	v_pk_fma_f32 v[24:25], v[24:25], s[18:19], v[12:13] op_sel_hi:[1,0,1]
	v_cvt_pk_bf16_f32 v59, v60, v61
	v_cvt_pk_bf16_f32 v60, v72, v73
	v_cvt_pk_bf16_f32 v61, v70, v71
	global_store_dwordx4 v[90:91], v[58:61], off offset:256
	v_pk_fma_f32 v[72:73], v[88:89], s[18:19], v[12:13] op_sel_hi:[1,0,1]
	s_and_b64 vcc, exec, s[6:7]
	v_add_u32_e32 v58, 0x80, v178
	v_mad_i64_i32 v[58:59], s[8:9], v58, s49, v[166:167]
	v_lshl_add_u64 v[70:71], v[58:59], 0, v[168:169]
	v_pk_fma_f32 v[58:59], v[94:95], s[18:19], v[14:15] op_sel_hi:[1,0,1]
	v_pk_fma_f32 v[60:61], v[96:97], s[18:19], v[16:17] op_sel_hi:[1,0,1]
	v_cvt_pk_bf16_f32 v58, v58, v59
	v_pk_fma_f32 v[14:15], v[30:31], s[18:19], v[14:15] op_sel_hi:[1,0,1]
	v_cvt_pk_bf16_f32 v59, v60, v61
	v_cvt_pk_bf16_f32 v60, v78, v79
	v_cvt_pk_bf16_f32 v61, v72, v73
	global_store_dwordx4 v[70:71], v[58:61], off
	v_pk_fma_f32 v[72:73], v[104:105], s[18:19], v[4:5] op_sel_hi:[1,0,1]
	v_pk_fma_f32 v[78:79], v[102:103], s[18:19], v[2:3] op_sel_hi:[1,0,1]
	v_pk_fma_f32 v[58:59], v[106:107], s[18:19], v[6:7] op_sel_hi:[1,0,1]
	v_pk_fma_f32 v[60:61], v[108:109], s[18:19], v[8:9] op_sel_hi:[1,0,1]
	v_cvt_pk_bf16_f32 v58, v58, v59
	s_mov_b32 s50, s14
	v_cvt_pk_bf16_f32 v59, v60, v61
	v_cvt_pk_bf16_f32 v60, v78, v79
	v_cvt_pk_bf16_f32 v61, v72, v73
	global_store_dwordx4 v[70:71], v[58:61], off offset:256
	s_mov_b32 s26, s20
	s_mov_b64 s[28:29], s[24:25]
	v_add_u32_e32 v58, 0x90, v178
	v_mad_i64_i32 v[58:59], s[8:9], v58, s49, v[166:167]
	v_lshl_add_u64 v[58:59], v[58:59], 0, v[168:169]
	v_pk_fma_f32 v[60:61], v[68:69], s[18:19], v[16:17] op_sel_hi:[1,0,1]
	v_pk_fma_f32 v[68:69], v[56:57], s[18:19], v[12:13] op_sel_hi:[1,0,1]
	v_pk_fma_f32 v[56:57], v[54:55], s[18:19], v[10:11] op_sel_hi:[1,0,1]
	v_cvt_pk_bf16_f32 v54, v66, v67
	v_cvt_pk_bf16_f32 v55, v60, v61
	v_pk_fma_f32 v[60:61], v[64:65], s[18:19], v[4:5] op_sel_hi:[1,0,1]
	v_cvt_pk_bf16_f32 v56, v56, v57
	v_cvt_pk_bf16_f32 v57, v68, v69
	global_store_dwordx4 v[58:59], v[54:57], off
	v_pk_fma_f32 v[16:17], v[32:33], s[18:19], v[16:17] op_sel_hi:[1,0,1]
	s_mov_b64 s[30:31], s[22:23]
	v_pk_fma_f32 v[54:55], v[74:75], s[18:19], v[6:7] op_sel_hi:[1,0,1]
	v_pk_fma_f32 v[56:57], v[76:77], s[18:19], v[8:9] op_sel_hi:[1,0,1]
	v_cvt_pk_bf16_f32 v54, v54, v55
	v_readlane_b32 s72, v254, 51
	v_cvt_pk_bf16_f32 v55, v56, v57
	v_cvt_pk_bf16_f32 v56, v62, v63
	v_cvt_pk_bf16_f32 v57, v60, v61
	global_store_dwordx4 v[58:59], v[54:57], off offset:256
	v_readlane_b32 s73, v254, 52
	s_nop 0
	v_add_u32_e32 v54, 0xa0, v178
	v_mad_i64_i32 v[54:55], s[8:9], v54, s49, v[166:167]
	v_lshl_add_u64 v[54:55], v[54:55], 0, v[168:169]
	v_pk_fma_f32 v[56:57], v[40:41], s[18:19], v[12:13] op_sel_hi:[1,0,1]
	v_pk_fma_f32 v[40:41], v[38:39], s[18:19], v[10:11] op_sel_hi:[1,0,1]
	v_cvt_pk_bf16_f32 v38, v46, v47
	v_cvt_pk_bf16_f32 v39, v48, v49
	v_pk_fma_f32 v[12:13], v[22:23], s[18:19], v[10:11] op_sel_hi:[1,0,1]
	v_cvt_pk_bf16_f32 v40, v40, v41
	v_cvt_pk_bf16_f32 v41, v56, v57
	global_store_dwordx4 v[54:55], v[38:41], off
	s_nop 1
	v_pk_fma_f32 v[38:39], v[50:51], s[18:19], v[6:7] op_sel_hi:[1,0,1]
	v_pk_fma_f32 v[40:41], v[52:53], s[18:19], v[8:9] op_sel_hi:[1,0,1]
	v_cvt_pk_bf16_f32 v38, v38, v39
	v_pk_fma_f32 v[8:9], v[36:37], s[18:19], v[8:9] op_sel_hi:[1,0,1]
	v_cvt_pk_bf16_f32 v39, v40, v41
	v_cvt_pk_bf16_f32 v40, v42, v43
	v_cvt_pk_bf16_f32 v41, v44, v45
	global_store_dwordx4 v[54:55], v[38:41], off offset:256
	v_cvt_pk_bf16_f32 v10, v14, v15
	v_cvt_pk_bf16_f32 v11, v16, v17
	v_cvt_pk_bf16_f32 v12, v12, v13
	v_cvt_pk_bf16_f32 v13, v24, v25
	v_pk_fma_f32 v[6:7], v[34:35], s[18:19], v[6:7] op_sel_hi:[1,0,1]
	s_nop 0
	v_add_u32_e32 v38, 0xb0, v178
	v_mad_i64_i32 v[38:39], s[8:9], v38, s49, v[166:167]
	v_lshl_add_u64 v[38:39], v[38:39], 0, v[168:169]
	global_store_dwordx4 v[38:39], v[10:13], off
	s_nop 1
	v_pk_fma_f32 v[10:11], v[28:29], s[18:19], v[4:5] op_sel_hi:[1,0,1]
	v_pk_fma_f32 v[4:5], v[26:27], s[18:19], v[2:3] op_sel_hi:[1,0,1]
	v_cvt_pk_bf16_f32 v2, v6, v7
	v_cvt_pk_bf16_f32 v3, v8, v9
	s_nop 0
	v_cvt_pk_bf16_f32 v4, v4, v5
	v_cvt_pk_bf16_f32 v5, v10, v11
	global_store_dwordx4 v[38:39], v[2:5], off offset:256
	s_cbranch_vccz .LBB0_212
	s_waitcnt vmcnt(0)
	v_readlane_b32 s44, v254, 43
	v_readlane_b32 s45, v254, 44
	s_cmpk_gt_u32 s19, 0xff
	s_mov_b64 s[52:53], s[44:45]
	v_readlane_b32 s46, v254, 45
	v_readlane_b32 s47, v254, 46
	s_cbranch_scc1 .LBB0_219
	s_barrier

.LBB0_1442:
	s_add_u32 s48, s96, s46
	s_addc_u32 s49, s97, s47
	s_add_u32 s50, s48, 0x32370200
	ds_read_b128 v[188:191], v176
	ds_read_b128 v[192:195], v176 offset:1024
	ds_read_b128 v[196:199], v176 offset:2048
	ds_read_b128 v[200:203], v176 offset:3072
	s_addc_u32 s51, s49, 0
	s_add_u32 s81, s78, s46
	s_addc_u32 s82, s79, s47
	s_cmpk_eq_i32 s46, 0x600
	s_cselect_b64 vcc, -1, 0
	s_and_b64 s[48:49], vcc, exec
	v_cndmask_b32_e32 v166, v184, v180, vcc
	s_cselect_b32 s51, s11, s51
	s_cselect_b32 s50, s10, s50
	v_cndmask_b32_e32 v252, v172, v182, vcc
	v_cndmask_b32_e32 v169, v168, v181, vcc
	v_cndmask_b32_e32 v171, v170, v183, vcc
	s_cselect_b32 s49, s39, s82
	s_cselect_b32 s48, s41, s81
	s_mov_b32 m0, s45
	v_lshl_add_u64 v[6:7], v[4:5], 0, s[46:47]
	ds_read_b128 v[10:13], v177
	ds_read_b128 v[14:17], v177 offset:1024
	ds_read_b128 v[204:207], v177 offset:2048
	ds_read_b128 v[208:211], v177 offset:3072
	ds_read_b128 v[212:215], v177 offset:4096
	ds_read_b128 v[216:219], v177 offset:5120
	ds_read_b128 v[220:223], v177 offset:6144
	ds_read_b128 v[224:227], v177 offset:7168
	global_load_lds_dwordx4 v[6:7], off
	v_lshl_add_u64 v[6:7], v[2:3], 0, s[46:47]
	s_mov_b32 m0, s69
	s_nop 0
	global_load_lds_dwordx4 v[6:7], off
	ds_read_b128 v[228:231], v178
	ds_read_b128 v[232:235], v178 offset:1024
	ds_read_b128 v[236:239], v178 offset:2048
	ds_read_b128 v[240:243], v178 offset:3072
	s_waitcnt vmcnt(8) lgkmcnt(0)
	s_barrier
	v_mfma_f32_16x16x128_f8f6f4 v[154:157], v[188:195], v[10:17], v[154:157]
	v_mfma_f32_16x16x128_f8f6f4 v[146:149], v[196:203], v[10:17], v[146:149]
	v_mfma_f32_16x16x128_f8f6f4 v[138:141], v[188:195], v[204:211], v[138:141]
	v_mfma_f32_16x16x128_f8f6f4 v[130:133], v[196:203], v[204:211], v[130:133]
	v_mfma_f32_16x16x128_f8f6f4 v[122:125], v[188:195], v[212:219], v[122:125]
	v_mfma_f32_16x16x128_f8f6f4 v[114:117], v[196:203], v[212:219], v[114:117]
	v_mfma_f32_16x16x128_f8f6f4 v[106:109], v[188:195], v[220:227], v[106:109]
	v_mfma_f32_16x16x128_f8f6f4 v[90:93], v[196:203], v[220:227], v[90:93]
	v_mfma_f32_16x16x128_f8f6f4 v[158:161], v[228:235], v[10:17], v[158:161]
	v_mfma_f32_16x16x128_f8f6f4 v[150:153], v[236:243], v[10:17], v[150:153]
	v_mfma_f32_16x16x128_f8f6f4 v[142:145], v[228:235], v[204:211], v[142:145]
	v_mfma_f32_16x16x128_f8f6f4 v[134:137], v[236:243], v[204:211], v[134:137]
	v_mfma_f32_16x16x128_f8f6f4 v[126:129], v[228:235], v[212:219], v[126:129]
	v_mfma_f32_16x16x128_f8f6f4 v[118:121], v[236:243], v[212:219], v[118:121]
	v_mfma_f32_16x16x128_f8f6f4 v[110:113], v[228:235], v[220:227], v[110:113]
	v_mfma_f32_16x16x128_f8f6f4 v[98:101], v[236:243], v[220:227], v[98:101]
	s_barrier
	ds_read_b128 v[204:207], v177 offset:16384
	ds_read_b128 v[208:211], v177 offset:17408
	ds_read_b128 v[212:215], v177 offset:18432
	ds_read_b128 v[216:219], v177 offset:19456
	ds_read_b128 v[220:223], v177 offset:20480
	ds_read_b128 v[224:227], v177 offset:21504
	ds_read_b128 v[244:247], v177 offset:22528
	ds_read_b128 v[248:251], v177 offset:23552
	s_mov_b32 m0, s70
	v_lshl_add_u64 v[6:7], s[48:49], 0, v[162:163]
	global_load_lds_dwordx4 v[6:7], off
	v_lshl_add_u64 v[8:9], s[48:49], 0, v[164:165]
	s_mov_b32 m0, s71
	s_nop 0
	global_load_lds_dwordx4 v[8:9], off
	s_mov_b32 m0, s55
	s_nop 0
	global_load_lds_dwordx4 v166, s[50:51]
	s_mov_b32 m0, s56
	v_mov_b32_e32 v253, v167
	global_load_lds_dwordx4 v252, s[50:51]
	s_add_u32 s82, s48, 0x40000
	s_addc_u32 s83, s49, 0
	s_mov_b32 m0, s72
	v_lshl_add_u64 v[14:15], s[82:83], 0, v[162:163]
	global_load_lds_dwordx4 v[14:15], off
	v_lshl_add_u64 v[14:15], s[82:83], 0, v[164:165]
	s_mov_b32 m0, s73
	s_nop 0
	global_load_lds_dwordx4 v[14:15], off
	s_waitcnt vmcnt(8) lgkmcnt(0)
	s_barrier
	v_lshl_add_u64 v[12:13], s[50:51], 0, v[166:167]
	v_lshl_add_u64 v[10:11], s[50:51], 0, v[252:253]
	v_mfma_f32_16x16x128_f8f6f4 v[94:97], v[188:195], v[204:211], v[94:97]
	v_mfma_f32_16x16x128_f8f6f4 v[82:85], v[196:203], v[204:211], v[82:85]
	v_mfma_f32_16x16x128_f8f6f4 v[74:77], v[188:195], v[212:219], v[74:77]
	v_mfma_f32_16x16x128_f8f6f4 v[66:69], v[196:203], v[212:219], v[66:69]
	v_mfma_f32_16x16x128_f8f6f4 v[58:61], v[188:195], v[220:227], v[58:61]
	v_mfma_f32_16x16x128_f8f6f4 v[50:53], v[196:203], v[220:227], v[50:53]
	v_mfma_f32_16x16x128_f8f6f4 v[42:45], v[188:195], v[244:251], v[42:45]
	v_mfma_f32_16x16x128_f8f6f4 v[34:37], v[196:203], v[244:251], v[34:37]
	v_mfma_f32_16x16x128_f8f6f4 v[102:105], v[228:235], v[204:211], v[102:105]
	v_mfma_f32_16x16x128_f8f6f4 v[86:89], v[236:243], v[204:211], v[86:89]
	v_mfma_f32_16x16x128_f8f6f4 v[78:81], v[228:235], v[212:219], v[78:81]
	v_mfma_f32_16x16x128_f8f6f4 v[70:73], v[236:243], v[212:219], v[70:73]
	v_mfma_f32_16x16x128_f8f6f4 v[62:65], v[228:235], v[220:227], v[62:65]
	v_mfma_f32_16x16x128_f8f6f4 v[54:57], v[236:243], v[220:227], v[54:57]
	v_mfma_f32_16x16x128_f8f6f4 v[46:49], v[228:235], v[244:251], v[46:49]
	v_mfma_f32_16x16x128_f8f6f4 v[38:41], v[236:243], v[244:251], v[38:41]
	s_barrier
	ds_read_b128 v[188:191], v185
	ds_read_b128 v[192:195], v185 offset:1024
	ds_read_b128 v[196:199], v185 offset:2048
	ds_read_b128 v[200:203], v185 offset:3072
	s_mov_b32 m0, s57
	ds_read_b128 v[204:207], v177 offset:32768
	ds_read_b128 v[208:211], v177 offset:33792
	ds_read_b128 v[212:215], v177 offset:34816
	ds_read_b128 v[216:219], v177 offset:35840
	ds_read_b128 v[220:223], v177 offset:36864
	ds_read_b128 v[224:227], v177 offset:37888
	ds_read_b128 v[228:231], v177 offset:38912
	ds_read_b128 v[232:235], v177 offset:39936
	global_load_lds_dwordx4 v169, s[50:51]
	s_mov_b32 m0, s58
	s_nop 0
	global_load_lds_dwordx4 v171, s[50:51]
	ds_read_b128 v[236:239], v186
	ds_read_b128 v[240:243], v186 offset:1024
	ds_read_b128 v[244:247], v186 offset:2048
	ds_read_b128 v[248:251], v186 offset:3072
	s_waitcnt vmcnt(8) lgkmcnt(0)
	s_barrier
	v_mfma_f32_16x16x128_f8f6f4 v[154:157], v[188:195], v[204:211], v[154:157]
	v_mfma_f32_16x16x128_f8f6f4 v[146:149], v[196:203], v[204:211], v[146:149]
	v_mfma_f32_16x16x128_f8f6f4 v[138:141], v[188:195], v[212:219], v[138:141]
	v_mfma_f32_16x16x128_f8f6f4 v[130:133], v[196:203], v[212:219], v[130:133]
	v_mfma_f32_16x16x128_f8f6f4 v[122:125], v[188:195], v[220:227], v[122:125]
	v_mfma_f32_16x16x128_f8f6f4 v[114:117], v[196:203], v[220:227], v[114:117]
	v_mfma_f32_16x16x128_f8f6f4 v[106:109], v[188:195], v[228:235], v[106:109]
	v_mfma_f32_16x16x128_f8f6f4 v[90:93], v[196:203], v[228:235], v[90:93]
	v_mfma_f32_16x16x128_f8f6f4 v[158:161], v[236:243], v[204:211], v[158:161]
	v_mfma_f32_16x16x128_f8f6f4 v[150:153], v[244:251], v[204:211], v[150:153]
	v_mfma_f32_16x16x128_f8f6f4 v[142:145], v[236:243], v[212:219], v[142:145]
	v_mfma_f32_16x16x128_f8f6f4 v[134:137], v[244:251], v[212:219], v[134:137]
	v_mfma_f32_16x16x128_f8f6f4 v[126:129], v[236:243], v[220:227], v[126:129]
	v_mfma_f32_16x16x128_f8f6f4 v[118:121], v[244:251], v[220:227], v[118:121]
	v_mfma_f32_16x16x128_f8f6f4 v[110:113], v[236:243], v[228:235], v[110:113]
	v_mfma_f32_16x16x128_f8f6f4 v[98:101], v[244:251], v[228:235], v[98:101]
	s_barrier
	ds_read_b128 v[204:207], v177 offset:49152
	ds_read_b128 v[208:211], v177 offset:50176
	ds_read_b128 v[212:215], v177 offset:51200
	ds_read_b128 v[216:219], v177 offset:52224
	ds_read_b128 v[220:223], v177 offset:53248
	ds_read_b128 v[224:227], v177 offset:54272
	ds_read_b128 v[228:231], v177 offset:55296
	ds_read_b128 v[232:235], v177 offset:56320
	s_mov_b32 m0, s74
	v_lshl_add_u64 v[6:7], v[6:7], 0, s[18:19]
	global_load_lds_dwordx4 v[6:7], off
	v_lshl_add_u64 v[6:7], v[8:9], 0, s[18:19]
	s_mov_b32 m0, s75
	s_nop 0
	global_load_lds_dwordx4 v[6:7], off
	s_mov_b32 m0, s60
	v_lshl_add_u64 v[6:7], v[12:13], 0, s[18:19]
	global_load_lds_dwordx4 v[6:7], off
	v_lshl_add_u64 v[6:7], v[10:11], 0, s[18:19]
	s_mov_b32 m0, s61
	s_nop 0
	global_load_lds_dwordx4 v[6:7], off
	s_add_u32 s48, s48, 0x40080
	s_addc_u32 s49, s49, 0
	s_mov_b32 m0, s76
	v_lshl_add_u64 v[6:7], s[48:49], 0, v[162:163]
	global_load_lds_dwordx4 v[6:7], off
	v_lshl_add_u64 v[6:7], s[48:49], 0, v[164:165]
	s_mov_b32 m0, s77
	s_nop 0
	global_load_lds_dwordx4 v[6:7], off
	s_waitcnt vmcnt(8) lgkmcnt(0)
	s_barrier
	v_mfma_f32_16x16x128_f8f6f4 v[94:97], v[188:195], v[204:211], v[94:97]
	v_mfma_f32_16x16x128_f8f6f4 v[82:85], v[196:203], v[204:211], v[82:85]
	v_mfma_f32_16x16x128_f8f6f4 v[74:77], v[188:195], v[212:219], v[74:77]
	v_mfma_f32_16x16x128_f8f6f4 v[66:69], v[196:203], v[212:219], v[66:69]
	v_mfma_f32_16x16x128_f8f6f4 v[58:61], v[188:195], v[220:227], v[58:61]
	v_mfma_f32_16x16x128_f8f6f4 v[50:53], v[196:203], v[220:227], v[50:53]
	v_mfma_f32_16x16x128_f8f6f4 v[42:45], v[188:195], v[228:235], v[42:45]
	v_mfma_f32_16x16x128_f8f6f4 v[34:37], v[196:203], v[228:235], v[34:37]
	v_mfma_f32_16x16x128_f8f6f4 v[102:105], v[236:243], v[204:211], v[102:105]
	v_mfma_f32_16x16x128_f8f6f4 v[86:89], v[244:251], v[204:211], v[86:89]
	v_mfma_f32_16x16x128_f8f6f4 v[78:81], v[236:243], v[212:219], v[78:81]
	v_mfma_f32_16x16x128_f8f6f4 v[70:73], v[244:251], v[212:219], v[70:73]
	v_mfma_f32_16x16x128_f8f6f4 v[62:65], v[236:243], v[220:227], v[62:65]
	v_mfma_f32_16x16x128_f8f6f4 v[54:57], v[244:251], v[220:227], v[54:57]
	v_mfma_f32_16x16x128_f8f6f4 v[46:49], v[236:243], v[228:235], v[46:49]
	v_mfma_f32_16x16x128_f8f6f4 v[38:41], v[244:251], v[228:235], v[38:41]
	s_add_i32 s80, s80, 2
	s_add_u32 s46, s46, 0x100
	s_addc_u32 s47, s47, 0
	s_cmp_gt_u32 s80, 13
	s_barrier
	s_cbranch_scc0 .LBB0_1442
	v_mov_b32_e32 v2, v0
	s_nop 15
	s_nop 15
	s_waitcnt vmcnt(6)
	s_lshl_b32 s41, s68, 8
	v_readfirstlane_b32 s39, v2
	v_pk_fma_f32 v[10:11], v[154:155], s[30:31], v[30:31] op_sel_hi:[1,0,1]
	s_ashr_i32 s45, s39, 2
	v_min_f32_e32 v10, 0x40e00000, v10
	v_min_f32_e32 v11, 0x40e00000, v11
	s_andn2_b32 s45, s45, 63
	v_pk_mul_f32 v[12:13], v[10:11], s[34:35] op_sel_hi:[1,0]
	s_add_i32 s45, s45, s41
	v_exp_f32_e32 v12, v12
	v_exp_f32_e32 v13, v13
	v_and_or_b32 v6, v2, 15, s45
	v_lshrrev_b32_e32 v2, 1, v2
	v_and_b32_e32 v8, 24, v2
	v_pk_fma_f32 v[2:3], v[156:157], s[30:31], v[32:33] op_sel_hi:[1,0,1]
	v_pk_add_f32 v[12:13], v[12:13], 1.0 op_sel_hi:[1,0]
	v_min_f32_e32 v2, 0x40e00000, v2
	v_min_f32_e32 v3, 0x40e00000, v3
	v_pk_mul_f32 v[154:155], v[2:3], s[34:35] op_sel_hi:[1,0]
	v_rcp_f32_e32 v12, v12
	v_rcp_f32_e32 v13, v13
	v_exp_f32_e32 v154, v154
	v_exp_f32_e32 v155, v155
	v_pk_fma_f32 v[16:17], v[158:159], s[30:31], v[26:27] op_sel_hi:[1,0,1]
	v_pk_fma_f32 v[14:15], v[160:161], s[30:31], v[28:29] op_sel_hi:[1,0,1]
	v_med3_f32 v16, v16, s65, v179
	v_med3_f32 v17, v17, s65, v179
	v_pk_fma_f32 v[10:11], v[16:17], v[10:11], v[10:11]
	v_med3_f32 v14, v14, s65, v179
	v_med3_f32 v15, v15, s65, v179
	v_pk_mul_f32 v[10:11], v[10:11], v[12:13]
	v_pk_add_f32 v[12:13], v[154:155], 1.0 op_sel_hi:[1,0]
	v_pk_fma_f32 v[2:3], v[14:15], v[2:3], v[2:3]
	v_pk_fma_f32 v[14:15], v[146:147], s[30:31], v[22:23] op_sel_hi:[1,0,1]
	v_rcp_f32_e32 v12, v12
	v_rcp_f32_e32 v13, v13
	v_min_f32_e32 v14, 0x40e00000, v14
	v_min_f32_e32 v15, 0x40e00000, v15
	v_pk_mul_f32 v[146:147], v[14:15], s[34:35] op_sel_hi:[1,0]
	v_pk_mul_f32 v[2:3], v[2:3], v[12:13]
	v_exp_f32_e32 v146, v146
	v_exp_f32_e32 v147, v147
	v_pk_fma_f32 v[12:13], v[148:149], s[30:31], v[24:25] op_sel_hi:[1,0,1]
	v_pk_fma_f32 v[148:149], v[150:151], s[30:31], v[18:19] op_sel_hi:[1,0,1]
	v_min_f32_e32 v12, 0x40e00000, v12
	v_med3_f32 v148, v148, s65, v179
	v_med3_f32 v149, v149, s65, v179
	v_min_f32_e32 v13, 0x40e00000, v13
	v_pk_add_f32 v[146:147], v[146:147], 1.0 op_sel_hi:[1,0]
	v_pk_fma_f32 v[14:15], v[148:149], v[14:15], v[14:15]
	v_pk_mul_f32 v[148:149], v[12:13], s[34:35] op_sel_hi:[1,0]
	v_rcp_f32_e32 v146, v146
	v_rcp_f32_e32 v147, v147
	v_exp_f32_e32 v148, v148
	v_exp_f32_e32 v149, v149
	v_pk_fma_f32 v[16:17], v[152:153], s[30:31], v[20:21] op_sel_hi:[1,0,1]
	v_pk_mul_f32 v[14:15], v[14:15], v[146:147]
	v_med3_f32 v16, v16, s65, v179
	v_pk_add_f32 v[146:147], v[148:149], 1.0 op_sel_hi:[1,0]
	v_mov_b32_e32 v149, v167
	v_cvt_pk_fp8_f32 v149, v14, v15
	v_pk_fma_f32 v[14:15], v[138:139], s[30:31], v[30:31] op_sel_hi:[1,0,1]
	v_med3_f32 v17, v17, s65, v179
	v_mov_b32_e32 v148, v167
	v_min_f32_e32 v14, 0x40e00000, v14
	v_min_f32_e32 v15, 0x40e00000, v15
	v_cvt_pk_fp8_f32 v148, v10, v11
	v_pk_fma_f32 v[10:11], v[16:17], v[12:13], v[12:13]
	v_pk_mul_f32 v[16:17], v[14:15], s[34:35] op_sel_hi:[1,0]
	v_pk_fma_f32 v[12:13], v[140:141], s[30:31], v[32:33] op_sel_hi:[1,0,1]
	v_exp_f32_e32 v16, v16
	v_exp_f32_e32 v17, v17
	v_min_f32_e32 v12, 0x40e00000, v12
	v_min_f32_e32 v13, 0x40e00000, v13
	v_pk_fma_f32 v[140:141], v[142:143], s[30:31], v[26:27] op_sel_hi:[1,0,1]
	v_pk_add_f32 v[16:17], v[16:17], 1.0 op_sel_hi:[1,0]
	v_pk_mul_f32 v[142:143], v[12:13], s[34:35] op_sel_hi:[1,0]
	v_rcp_f32_e32 v16, v16
	v_rcp_f32_e32 v17, v17
	v_exp_f32_e32 v142, v142
	v_exp_f32_e32 v143, v143
	v_med3_f32 v140, v140, s65, v179
	v_med3_f32 v141, v141, s65, v179
	v_pk_fma_f32 v[14:15], v[140:141], v[14:15], v[14:15]
	v_pk_fma_f32 v[138:139], v[144:145], s[30:31], v[28:29] op_sel_hi:[1,0,1]
	v_pk_mul_f32 v[14:15], v[14:15], v[16:17]
	v_pk_add_f32 v[16:17], v[142:143], 1.0 op_sel_hi:[1,0]
	v_med3_f32 v138, v138, s65, v179
	v_rcp_f32_e32 v16, v16
	v_rcp_f32_e32 v17, v17
	v_med3_f32 v139, v139, s65, v179
	v_pk_fma_f32 v[130:131], v[130:131], s[30:31], v[22:23] op_sel_hi:[1,0,1]
	v_pk_fma_f32 v[12:13], v[138:139], v[12:13], v[12:13]
	v_min_f32_e32 v130, 0x40e00000, v130
	v_min_f32_e32 v131, 0x40e00000, v131
	v_pk_mul_f32 v[12:13], v[12:13], v[16:17]
	v_pk_fma_f32 v[16:17], v[132:133], s[30:31], v[24:25] op_sel_hi:[1,0,1]
	v_pk_fma_f32 v[132:133], v[136:137], s[30:31], v[20:21] op_sel_hi:[1,0,1]
	v_pk_mul_f32 v[136:137], v[130:131], s[34:35] op_sel_hi:[1,0]
	v_pk_fma_f32 v[134:135], v[134:135], s[30:31], v[18:19] op_sel_hi:[1,0,1]
	v_exp_f32_e32 v136, v136
	v_exp_f32_e32 v137, v137
	v_med3_f32 v134, v134, s65, v179
	v_med3_f32 v135, v135, s65, v179
	v_min_f32_e32 v16, 0x40e00000, v16
	v_min_f32_e32 v17, 0x40e00000, v17
	v_pk_fma_f32 v[130:131], v[134:135], v[130:131], v[130:131]
	v_pk_mul_f32 v[134:135], v[16:17], s[34:35] op_sel_hi:[1,0]
	v_pk_add_f32 v[136:137], v[136:137], 1.0 op_sel_hi:[1,0]
	v_exp_f32_e32 v134, v134
	v_exp_f32_e32 v135, v135
	v_rcp_f32_e32 v136, v136
	v_rcp_f32_e32 v137, v137
	v_med3_f32 v132, v132, s65, v179
	v_pk_add_f32 v[134:135], v[134:135], 1.0 op_sel_hi:[1,0]
	v_med3_f32 v133, v133, s65, v179
	v_pk_mul_f32 v[130:131], v[130:131], v[136:137]
	v_rcp_f32_e32 v134, v134
	v_rcp_f32_e32 v135, v135
	v_mov_b32_e32 v137, v167
	v_cvt_pk_fp8_f32 v137, v130, v131
	v_mov_b32_e32 v136, v167
	v_cvt_pk_fp8_f32 v136, v14, v15
	v_pk_fma_f32 v[14:15], v[132:133], v[16:17], v[16:17]
	v_pk_fma_f32 v[114:115], v[114:115], s[30:31], v[22:23] op_sel_hi:[1,0,1]
	v_pk_mul_f32 v[14:15], v[14:15], v[134:135]
	v_cvt_pk_fp8_f32 v136, v12, v13 op_sel:[0,0,1]
	v_cvt_pk_fp8_f32 v137, v14, v15 op_sel:[0,0,1]
	v_pk_fma_f32 v[14:15], v[122:123], s[30:31], v[30:31] op_sel_hi:[1,0,1]
	v_pk_fma_f32 v[12:13], v[124:125], s[30:31], v[32:33] op_sel_hi:[1,0,1]
	v_min_f32_e32 v14, 0x40e00000, v14
	v_min_f32_e32 v15, 0x40e00000, v15
	v_pk_mul_f32 v[16:17], v[14:15], s[34:35] op_sel_hi:[1,0]
	v_min_f32_e32 v12, 0x40e00000, v12
	v_exp_f32_e32 v16, v16
	v_exp_f32_e32 v17, v17
	v_min_f32_e32 v13, 0x40e00000, v13
	v_pk_fma_f32 v[124:125], v[126:127], s[30:31], v[26:27] op_sel_hi:[1,0,1]
	v_pk_mul_f32 v[126:127], v[12:13], s[34:35] op_sel_hi:[1,0]
	v_pk_add_f32 v[16:17], v[16:17], 1.0 op_sel_hi:[1,0]
	v_exp_f32_e32 v126, v126
	v_rcp_f32_e32 v16, v16
	v_rcp_f32_e32 v17, v17
	v_exp_f32_e32 v127, v127
	v_med3_f32 v124, v124, s65, v179
	v_med3_f32 v125, v125, s65, v179
	v_pk_fma_f32 v[14:15], v[124:125], v[14:15], v[14:15]
	v_pk_fma_f32 v[122:123], v[128:129], s[30:31], v[28:29] op_sel_hi:[1,0,1]
	v_pk_mul_f32 v[14:15], v[14:15], v[16:17]
	v_pk_add_f32 v[16:17], v[126:127], 1.0 op_sel_hi:[1,0]
	v_med3_f32 v122, v122, s65, v179
	v_rcp_f32_e32 v16, v16
	v_rcp_f32_e32 v17, v17
	v_med3_f32 v123, v123, s65, v179
	v_pk_fma_f32 v[12:13], v[122:123], v[12:13], v[12:13]
	v_min_f32_e32 v114, 0x40e00000, v114
	v_min_f32_e32 v115, 0x40e00000, v115
	v_pk_mul_f32 v[12:13], v[12:13], v[16:17]
	v_pk_fma_f32 v[16:17], v[116:117], s[30:31], v[24:25] op_sel_hi:[1,0,1]
	v_pk_fma_f32 v[116:117], v[120:121], s[30:31], v[20:21] op_sel_hi:[1,0,1]
	v_pk_mul_f32 v[120:121], v[114:115], s[34:35] op_sel_hi:[1,0]
	v_pk_fma_f32 v[118:119], v[118:119], s[30:31], v[18:19] op_sel_hi:[1,0,1]
	v_exp_f32_e32 v120, v120
	v_exp_f32_e32 v121, v121
	v_med3_f32 v118, v118, s65, v179
	v_med3_f32 v119, v119, s65, v179
	v_min_f32_e32 v16, 0x40e00000, v16
	v_min_f32_e32 v17, 0x40e00000, v17
	v_rcp_f32_e32 v146, v146
	v_rcp_f32_e32 v147, v147
	v_pk_add_f32 v[120:121], v[120:121], 1.0 op_sel_hi:[1,0]
	v_pk_fma_f32 v[114:115], v[118:119], v[114:115], v[114:115]
	v_pk_mul_f32 v[118:119], v[16:17], s[34:35] op_sel_hi:[1,0]
	v_rcp_f32_e32 v120, v120
	v_rcp_f32_e32 v121, v121
	v_exp_f32_e32 v118, v118
	v_exp_f32_e32 v119, v119
	s_lshr_b32 s39, s39, 1
	v_pk_mul_f32 v[10:11], v[10:11], v[146:147]
	s_lshl_b32 s41, s44, 7
	s_and_b32 s39, s39, 0x60
	v_cvt_pk_fp8_f32 v149, v10, v11 op_sel:[0,0,1]
	v_or_b32_e32 v10, 16, v6
	v_pk_mul_f32 v[114:115], v[114:115], v[120:121]
	v_pk_add_f32 v[118:119], v[118:119], 1.0 op_sel_hi:[1,0]
	v_mov_b32_e32 v120, v167
	s_or_b32 s41, s39, s41
	v_ashrrev_i32_e32 v11, 31, v10
	v_rcp_f32_e32 v118, v118
	v_rcp_f32_e32 v119, v119
	v_cvt_pk_fp8_f32 v120, v14, v15
	v_mov_b32_e32 v121, v167
	v_or_b32_e32 v4, s41, v8
	v_lshlrev_b64 v[10:11], 11, v[10:11]
	v_cvt_pk_fp8_f32 v121, v114, v115
	v_ashrrev_i32_e32 v5, 31, v4
	v_lshl_add_u64 v[10:11], s[16:17], 0, v[10:11]
	v_med3_f32 v116, v116, s65, v179
	v_med3_f32 v117, v117, s65, v179
	v_lshl_add_u64 v[10:11], v[10:11], 0, v[4:5]
	v_pk_fma_f32 v[14:15], v[116:117], v[16:17], v[16:17]
	global_store_dwordx2 v[10:11], v[136:137], off
	v_or_b32_e32 v10, 32, v6
	v_pk_mul_f32 v[14:15], v[14:15], v[118:119]
	v_cvt_pk_fp8_f32 v120, v12, v13 op_sel:[0,0,1]
	v_pk_fma_f32 v[12:13], v[106:107], s[30:31], v[30:31] op_sel_hi:[1,0,1]
	v_ashrrev_i32_e32 v11, 31, v10
	v_cvt_pk_fp8_f32 v121, v14, v15 op_sel:[0,0,1]
	v_min_f32_e32 v12, 0x40e00000, v12
	v_min_f32_e32 v13, 0x40e00000, v13
	v_lshlrev_b64 v[10:11], 11, v[10:11]
	v_pk_mul_f32 v[14:15], v[12:13], s[34:35] op_sel_hi:[1,0]
	v_lshl_add_u64 v[10:11], s[16:17], 0, v[10:11]
	v_exp_f32_e32 v14, v14
	v_exp_f32_e32 v15, v15
	v_lshl_add_u64 v[10:11], v[10:11], 0, v[4:5]
	global_store_dwordx2 v[10:11], v[120:121], off
	v_pk_fma_f32 v[10:11], v[108:109], s[30:31], v[32:33] op_sel_hi:[1,0,1]
	v_pk_add_f32 v[14:15], v[14:15], 1.0 op_sel_hi:[1,0]
	v_min_f32_e32 v10, 0x40e00000, v10
	v_min_f32_e32 v11, 0x40e00000, v11
	v_pk_mul_f32 v[108:109], v[10:11], s[34:35] op_sel_hi:[1,0]
	v_rcp_f32_e32 v14, v14
	v_rcp_f32_e32 v15, v15
	v_exp_f32_e32 v108, v108
	v_exp_f32_e32 v109, v109
	v_pk_fma_f32 v[106:107], v[110:111], s[30:31], v[26:27] op_sel_hi:[1,0,1]
	v_pk_fma_f32 v[16:17], v[112:113], s[30:31], v[28:29] op_sel_hi:[1,0,1]
	v_med3_f32 v106, v106, s65, v179
	v_med3_f32 v107, v107, s65, v179
	v_pk_fma_f32 v[12:13], v[106:107], v[12:13], v[12:13]
	v_med3_f32 v16, v16, s65, v179
	v_pk_mul_f32 v[12:13], v[12:13], v[14:15]
	v_pk_add_f32 v[14:15], v[108:109], 1.0 op_sel_hi:[1,0]
	v_med3_f32 v17, v17, s65, v179
	v_rcp_f32_e32 v14, v14
	v_rcp_f32_e32 v15, v15
	v_pk_fma_f32 v[10:11], v[16:17], v[10:11], v[10:11]
	v_pk_fma_f32 v[16:17], v[90:91], s[30:31], v[22:23] op_sel_hi:[1,0,1]
	v_pk_fma_f32 v[98:99], v[98:99], s[30:31], v[18:19] op_sel_hi:[1,0,1]
	v_min_f32_e32 v16, 0x40e00000, v16
	v_min_f32_e32 v17, 0x40e00000, v17
	v_pk_mul_f32 v[10:11], v[10:11], v[14:15]
	v_pk_fma_f32 v[14:15], v[92:93], s[30:31], v[24:25] op_sel_hi:[1,0,1]
	v_pk_mul_f32 v[92:93], v[16:17], s[34:35] op_sel_hi:[1,0]
	v_med3_f32 v98, v98, s65, v179
	v_exp_f32_e32 v92, v92
	v_exp_f32_e32 v93, v93
	v_med3_f32 v99, v99, s65, v179
	v_min_f32_e32 v14, 0x40e00000, v14
	v_min_f32_e32 v15, 0x40e00000, v15
	v_pk_add_f32 v[92:93], v[92:93], 1.0 op_sel_hi:[1,0]
	v_pk_fma_f32 v[16:17], v[98:99], v[16:17], v[16:17]
	v_pk_mul_f32 v[98:99], v[14:15], s[34:35] op_sel_hi:[1,0]
	v_rcp_f32_e32 v92, v92
	v_rcp_f32_e32 v93, v93
	v_exp_f32_e32 v98, v98
	v_exp_f32_e32 v99, v99
	v_ashrrev_i32_e32 v7, 31, v6
	v_pk_mul_f32 v[16:17], v[16:17], v[92:93]
	v_cvt_pk_fp8_f32 v148, v2, v3 op_sel:[0,0,1]
	v_pk_add_f32 v[92:93], v[98:99], 1.0 op_sel_hi:[1,0]
	v_lshlrev_b64 v[2:3], 11, v[6:7]
	v_or_b32_e32 v6, 48, v6
	v_rcp_f32_e32 v92, v92
	v_rcp_f32_e32 v93, v93
	v_mov_b32_e32 v98, v167
	v_mov_b32_e32 v99, v167
	v_ashrrev_i32_e32 v7, 31, v6
	v_pk_fma_f32 v[90:91], v[100:101], s[30:31], v[20:21] op_sel_hi:[1,0,1]
	v_cvt_pk_fp8_f32 v98, v12, v13
	v_cvt_pk_fp8_f32 v99, v16, v17
	v_med3_f32 v90, v90, s65, v179
	v_med3_f32 v91, v91, s65, v179
	v_lshlrev_b64 v[6:7], 11, v[6:7]
	v_lshl_add_u64 v[2:3], s[16:17], 0, v[2:3]
	v_pk_fma_f32 v[12:13], v[90:91], v[14:15], v[14:15]
	v_lshl_add_u64 v[6:7], s[16:17], 0, v[6:7]
	v_lshl_add_u64 v[2:3], v[2:3], 0, v[4:5]
	v_pk_mul_f32 v[12:13], v[12:13], v[92:93]
	v_lshl_add_u64 v[4:5], v[6:7], 0, v[4:5]
	v_pk_fma_f32 v[6:7], v[94:95], s[30:31], v[30:31] op_sel_hi:[1,0,1]
	v_cvt_pk_fp8_f32 v98, v10, v11 op_sel:[0,0,1]
	v_cvt_pk_fp8_f32 v99, v12, v13 op_sel:[0,0,1]
	v_min_f32_e32 v6, 0x40e00000, v6
	v_min_f32_e32 v7, 0x40e00000, v7
	v_pk_mul_f32 v[10:11], v[6:7], s[34:35] op_sel_hi:[1,0]
	global_store_dwordx2 v[4:5], v[98:99], off
	v_exp_f32_e32 v10, v10
	v_exp_f32_e32 v11, v11
	v_pk_fma_f32 v[4:5], v[96:97], s[30:31], v[32:33] op_sel_hi:[1,0,1]
	v_pk_fma_f32 v[14:15], v[102:103], s[30:31], v[26:27] op_sel_hi:[1,0,1]
	v_min_f32_e32 v4, 0x40e00000, v4
	v_min_f32_e32 v5, 0x40e00000, v5
	v_pk_add_f32 v[10:11], v[10:11], 1.0 op_sel_hi:[1,0]
	v_pk_mul_f32 v[16:17], v[4:5], s[34:35] op_sel_hi:[1,0]
	v_rcp_f32_e32 v10, v10
	v_rcp_f32_e32 v11, v11
	v_exp_f32_e32 v16, v16
	v_exp_f32_e32 v17, v17
	v_pk_fma_f32 v[12:13], v[104:105], s[30:31], v[28:29] op_sel_hi:[1,0,1]
	v_med3_f32 v14, v14, s65, v179
	v_med3_f32 v15, v15, s65, v179
	v_pk_fma_f32 v[6:7], v[14:15], v[6:7], v[6:7]
	v_med3_f32 v12, v12, s65, v179
	v_med3_f32 v13, v13, s65, v179
	v_pk_mul_f32 v[6:7], v[6:7], v[10:11]
	v_pk_add_f32 v[10:11], v[16:17], 1.0 op_sel_hi:[1,0]
	v_pk_fma_f32 v[4:5], v[12:13], v[4:5], v[4:5]
	v_pk_fma_f32 v[12:13], v[82:83], s[30:31], v[22:23] op_sel_hi:[1,0,1]
	v_rcp_f32_e32 v10, v10
	v_rcp_f32_e32 v11, v11
	v_min_f32_e32 v12, 0x40e00000, v12
	v_min_f32_e32 v13, 0x40e00000, v13
	v_pk_mul_f32 v[16:17], v[12:13], s[34:35] op_sel_hi:[1,0]
	v_pk_mul_f32 v[4:5], v[4:5], v[10:11]
	v_exp_f32_e32 v16, v16
	v_exp_f32_e32 v17, v17
	v_pk_fma_f32 v[10:11], v[84:85], s[30:31], v[24:25] op_sel_hi:[1,0,1]
	v_pk_fma_f32 v[82:83], v[86:87], s[30:31], v[18:19] op_sel_hi:[1,0,1]
	v_min_f32_e32 v10, 0x40e00000, v10
	v_med3_f32 v82, v82, s65, v179
	v_med3_f32 v83, v83, s65, v179
	v_min_f32_e32 v11, 0x40e00000, v11
	v_pk_add_f32 v[16:17], v[16:17], 1.0 op_sel_hi:[1,0]
	v_pk_fma_f32 v[12:13], v[82:83], v[12:13], v[12:13]
	v_pk_mul_f32 v[82:83], v[10:11], s[34:35] op_sel_hi:[1,0]
	v_rcp_f32_e32 v16, v16
	v_rcp_f32_e32 v17, v17
	v_exp_f32_e32 v82, v82
	v_exp_f32_e32 v83, v83
	v_pk_fma_f32 v[14:15], v[88:89], s[30:31], v[20:21] op_sel_hi:[1,0,1]
	v_pk_mul_f32 v[12:13], v[12:13], v[16:17]
	v_med3_f32 v14, v14, s65, v179
	v_pk_add_f32 v[16:17], v[82:83], 1.0 op_sel_hi:[1,0]
	v_mov_b32_e32 v83, v167
	v_rcp_f32_e32 v16, v16
	v_rcp_f32_e32 v17, v17
	v_mov_b32_e32 v82, v167
	v_cvt_pk_fp8_f32 v83, v12, v13
	v_med3_f32 v15, v15, s65, v179
	v_cvt_pk_fp8_f32 v82, v6, v7
	v_pk_fma_f32 v[6:7], v[14:15], v[10:11], v[10:11]
	s_mov_b32 s41, 0x40000
	v_pk_mul_f32 v[6:7], v[6:7], v[16:17]
	v_cvt_pk_fp8_f32 v82, v4, v5 op_sel:[0,0,1]
	v_cvt_pk_fp8_f32 v83, v6, v7 op_sel:[0,0,1]
	v_pk_fma_f32 v[6:7], v[74:75], s[30:31], v[30:31] op_sel_hi:[1,0,1]
	v_add_co_u32_e32 v4, vcc, s41, v2
	v_min_f32_e32 v6, 0x40e00000, v6
	v_min_f32_e32 v7, 0x40e00000, v7
	v_pk_mul_f32 v[10:11], v[6:7], s[34:35] op_sel_hi:[1,0]
	v_addc_co_u32_e32 v5, vcc, 0, v3, vcc
	v_exp_f32_e32 v10, v10
	v_exp_f32_e32 v11, v11
	global_store_dwordx2 v[4:5], v[82:83], off
	v_pk_fma_f32 v[4:5], v[76:77], s[30:31], v[32:33] op_sel_hi:[1,0,1]
	v_pk_fma_f32 v[14:15], v[78:79], s[30:31], v[26:27] op_sel_hi:[1,0,1]
	v_min_f32_e32 v4, 0x40e00000, v4
	v_min_f32_e32 v5, 0x40e00000, v5
	v_pk_add_f32 v[10:11], v[10:11], 1.0 op_sel_hi:[1,0]
	v_pk_mul_f32 v[16:17], v[4:5], s[34:35] op_sel_hi:[1,0]
	v_rcp_f32_e32 v10, v10
	v_rcp_f32_e32 v11, v11
	v_exp_f32_e32 v16, v16
	v_exp_f32_e32 v17, v17
	v_pk_fma_f32 v[12:13], v[80:81], s[30:31], v[28:29] op_sel_hi:[1,0,1]
	v_med3_f32 v14, v14, s65, v179
	v_med3_f32 v15, v15, s65, v179
	v_pk_fma_f32 v[6:7], v[14:15], v[6:7], v[6:7]
	v_med3_f32 v12, v12, s65, v179
	v_med3_f32 v13, v13, s65, v179
	v_pk_mul_f32 v[6:7], v[6:7], v[10:11]
	v_pk_add_f32 v[10:11], v[16:17], 1.0 op_sel_hi:[1,0]
	v_pk_fma_f32 v[4:5], v[12:13], v[4:5], v[4:5]
	v_pk_fma_f32 v[12:13], v[66:67], s[30:31], v[22:23] op_sel_hi:[1,0,1]
	v_rcp_f32_e32 v10, v10
	v_rcp_f32_e32 v11, v11
	v_min_f32_e32 v12, 0x40e00000, v12
	v_min_f32_e32 v13, 0x40e00000, v13
	v_pk_mul_f32 v[16:17], v[12:13], s[34:35] op_sel_hi:[1,0]
	v_pk_mul_f32 v[4:5], v[4:5], v[10:11]
	v_exp_f32_e32 v16, v16
	v_exp_f32_e32 v17, v17
	v_pk_fma_f32 v[10:11], v[68:69], s[30:31], v[24:25] op_sel_hi:[1,0,1]
	v_pk_fma_f32 v[66:67], v[70:71], s[30:31], v[18:19] op_sel_hi:[1,0,1]
	v_min_f32_e32 v10, 0x40e00000, v10
	v_med3_f32 v66, v66, s65, v179
	v_med3_f32 v67, v67, s65, v179
	v_min_f32_e32 v11, 0x40e00000, v11
	v_pk_add_f32 v[16:17], v[16:17], 1.0 op_sel_hi:[1,0]
	v_pk_fma_f32 v[12:13], v[66:67], v[12:13], v[12:13]
	v_pk_mul_f32 v[66:67], v[10:11], s[34:35] op_sel_hi:[1,0]
	v_rcp_f32_e32 v16, v16
	v_rcp_f32_e32 v17, v17
	v_exp_f32_e32 v66, v66
	v_exp_f32_e32 v67, v67
	v_pk_fma_f32 v[14:15], v[72:73], s[30:31], v[20:21] op_sel_hi:[1,0,1]
	v_pk_mul_f32 v[12:13], v[12:13], v[16:17]
	v_med3_f32 v14, v14, s65, v179
	v_pk_add_f32 v[16:17], v[66:67], 1.0 op_sel_hi:[1,0]
	v_mov_b32_e32 v67, v167
	v_rcp_f32_e32 v16, v16
	v_rcp_f32_e32 v17, v17
	v_mov_b32_e32 v66, v167
	v_cvt_pk_fp8_f32 v67, v12, v13
	v_med3_f32 v15, v15, s65, v179
	v_cvt_pk_fp8_f32 v66, v6, v7
	v_pk_fma_f32 v[6:7], v[14:15], v[10:11], v[10:11]
	s_mov_b32 s41, 0x48000
	v_pk_mul_f32 v[6:7], v[6:7], v[16:17]
	v_cvt_pk_fp8_f32 v66, v4, v5 op_sel:[0,0,1]
	v_cvt_pk_fp8_f32 v67, v6, v7 op_sel:[0,0,1]
	v_pk_fma_f32 v[6:7], v[58:59], s[30:31], v[30:31] op_sel_hi:[1,0,1]
	v_add_co_u32_e32 v4, vcc, s41, v2
	v_min_f32_e32 v6, 0x40e00000, v6
	v_min_f32_e32 v7, 0x40e00000, v7
	v_pk_mul_f32 v[10:11], v[6:7], s[34:35] op_sel_hi:[1,0]
	v_addc_co_u32_e32 v5, vcc, 0, v3, vcc
	v_exp_f32_e32 v10, v10
	v_exp_f32_e32 v11, v11
	global_store_dwordx2 v[4:5], v[66:67], off
	v_pk_fma_f32 v[4:5], v[60:61], s[30:31], v[32:33] op_sel_hi:[1,0,1]
	v_pk_fma_f32 v[14:15], v[62:63], s[30:31], v[26:27] op_sel_hi:[1,0,1]
	v_min_f32_e32 v4, 0x40e00000, v4
	v_min_f32_e32 v5, 0x40e00000, v5
	v_pk_add_f32 v[10:11], v[10:11], 1.0 op_sel_hi:[1,0]
	v_pk_mul_f32 v[16:17], v[4:5], s[34:35] op_sel_hi:[1,0]
	v_rcp_f32_e32 v10, v10
	v_rcp_f32_e32 v11, v11
	v_exp_f32_e32 v16, v16
	v_exp_f32_e32 v17, v17
	v_pk_fma_f32 v[12:13], v[64:65], s[30:31], v[28:29] op_sel_hi:[1,0,1]
	v_med3_f32 v14, v14, s65, v179
	v_med3_f32 v15, v15, s65, v179
	v_pk_fma_f32 v[6:7], v[14:15], v[6:7], v[6:7]
	v_med3_f32 v12, v12, s65, v179
	v_med3_f32 v13, v13, s65, v179
	v_pk_mul_f32 v[6:7], v[6:7], v[10:11]
	v_pk_add_f32 v[10:11], v[16:17], 1.0 op_sel_hi:[1,0]
	v_pk_fma_f32 v[4:5], v[12:13], v[4:5], v[4:5]
	v_pk_fma_f32 v[12:13], v[50:51], s[30:31], v[22:23] op_sel_hi:[1,0,1]
	v_rcp_f32_e32 v10, v10
	v_rcp_f32_e32 v11, v11
	v_min_f32_e32 v12, 0x40e00000, v12
	v_min_f32_e32 v13, 0x40e00000, v13
	v_pk_mul_f32 v[16:17], v[12:13], s[34:35] op_sel_hi:[1,0]
	v_pk_mul_f32 v[4:5], v[4:5], v[10:11]
	v_exp_f32_e32 v16, v16
	v_exp_f32_e32 v17, v17
	v_pk_fma_f32 v[10:11], v[52:53], s[30:31], v[24:25] op_sel_hi:[1,0,1]
	v_pk_fma_f32 v[50:51], v[54:55], s[30:31], v[18:19] op_sel_hi:[1,0,1]
	v_min_f32_e32 v10, 0x40e00000, v10
	v_med3_f32 v50, v50, s65, v179
	v_med3_f32 v51, v51, s65, v179
	v_min_f32_e32 v11, 0x40e00000, v11
	v_pk_add_f32 v[16:17], v[16:17], 1.0 op_sel_hi:[1,0]
	v_pk_fma_f32 v[12:13], v[50:51], v[12:13], v[12:13]
	v_pk_mul_f32 v[50:51], v[10:11], s[34:35] op_sel_hi:[1,0]
	v_rcp_f32_e32 v16, v16
	v_rcp_f32_e32 v17, v17
	v_exp_f32_e32 v50, v50
	v_exp_f32_e32 v51, v51
	v_pk_fma_f32 v[14:15], v[56:57], s[30:31], v[20:21] op_sel_hi:[1,0,1]
	v_pk_mul_f32 v[12:13], v[12:13], v[16:17]
	v_med3_f32 v14, v14, s65, v179
	v_pk_add_f32 v[16:17], v[50:51], 1.0 op_sel_hi:[1,0]
	v_mov_b32_e32 v51, v167
	v_rcp_f32_e32 v16, v16
	v_rcp_f32_e32 v17, v17
	v_mov_b32_e32 v50, v167
	v_cvt_pk_fp8_f32 v51, v12, v13
	v_med3_f32 v15, v15, s65, v179
	v_cvt_pk_fp8_f32 v50, v6, v7
	v_pk_fma_f32 v[6:7], v[14:15], v[10:11], v[10:11]
	s_mov_b32 s41, 0x50000
	v_pk_mul_f32 v[6:7], v[6:7], v[16:17]
	v_cvt_pk_fp8_f32 v50, v4, v5 op_sel:[0,0,1]
	v_cvt_pk_fp8_f32 v51, v6, v7 op_sel:[0,0,1]
	v_pk_fma_f32 v[6:7], v[42:43], s[30:31], v[30:31] op_sel_hi:[1,0,1]
	v_add_co_u32_e32 v4, vcc, s41, v2
	v_min_f32_e32 v6, 0x40e00000, v6
	v_min_f32_e32 v7, 0x40e00000, v7
	v_pk_mul_f32 v[10:11], v[6:7], s[34:35] op_sel_hi:[1,0]
	v_addc_co_u32_e32 v5, vcc, 0, v3, vcc
	v_exp_f32_e32 v10, v10
	v_exp_f32_e32 v11, v11
	global_store_dwordx2 v[4:5], v[50:51], off
	v_pk_fma_f32 v[4:5], v[44:45], s[30:31], v[32:33] op_sel_hi:[1,0,1]
	v_pk_fma_f32 v[14:15], v[46:47], s[30:31], v[26:27] op_sel_hi:[1,0,1]
	v_min_f32_e32 v4, 0x40e00000, v4
	v_min_f32_e32 v5, 0x40e00000, v5
	v_pk_add_f32 v[10:11], v[10:11], 1.0 op_sel_hi:[1,0]
	v_pk_mul_f32 v[16:17], v[4:5], s[34:35] op_sel_hi:[1,0]
	v_rcp_f32_e32 v10, v10
	v_rcp_f32_e32 v11, v11
	v_exp_f32_e32 v16, v16
	v_exp_f32_e32 v17, v17
	v_pk_fma_f32 v[12:13], v[48:49], s[30:31], v[28:29] op_sel_hi:[1,0,1]
	v_med3_f32 v14, v14, s65, v179
	v_med3_f32 v15, v15, s65, v179
	v_pk_fma_f32 v[6:7], v[14:15], v[6:7], v[6:7]
	v_med3_f32 v12, v12, s65, v179
	v_med3_f32 v13, v13, s65, v179
	v_pk_mul_f32 v[6:7], v[6:7], v[10:11]
	v_pk_add_f32 v[10:11], v[16:17], 1.0 op_sel_hi:[1,0]
	v_pk_fma_f32 v[4:5], v[12:13], v[4:5], v[4:5]
	v_pk_fma_f32 v[12:13], v[34:35], s[30:31], v[22:23] op_sel_hi:[1,0,1]
	v_rcp_f32_e32 v10, v10
	v_rcp_f32_e32 v11, v11
	v_min_f32_e32 v12, 0x40e00000, v12
	v_min_f32_e32 v13, 0x40e00000, v13
	v_pk_mul_f32 v[16:17], v[12:13], s[34:35] op_sel_hi:[1,0]
	v_pk_mul_f32 v[4:5], v[4:5], v[10:11]
	v_exp_f32_e32 v16, v16
	v_exp_f32_e32 v17, v17
	v_pk_fma_f32 v[10:11], v[36:37], s[30:31], v[24:25] op_sel_hi:[1,0,1]
	v_pk_fma_f32 v[18:19], v[38:39], s[30:31], v[18:19] op_sel_hi:[1,0,1]
	v_min_f32_e32 v10, 0x40e00000, v10
	v_med3_f32 v18, v18, s65, v179
	v_med3_f32 v19, v19, s65, v179
	v_min_f32_e32 v11, 0x40e00000, v11
	v_pk_add_f32 v[16:17], v[16:17], 1.0 op_sel_hi:[1,0]
	v_pk_fma_f32 v[12:13], v[18:19], v[12:13], v[12:13]
	v_pk_mul_f32 v[18:19], v[10:11], s[34:35] op_sel_hi:[1,0]
	v_rcp_f32_e32 v16, v16
	v_rcp_f32_e32 v17, v17
	v_exp_f32_e32 v18, v18
	v_exp_f32_e32 v19, v19
	v_pk_fma_f32 v[14:15], v[40:41], s[30:31], v[20:21] op_sel_hi:[1,0,1]
	v_pk_mul_f32 v[12:13], v[12:13], v[16:17]
	v_med3_f32 v14, v14, s65, v179
	v_pk_add_f32 v[16:17], v[18:19], 1.0 op_sel_hi:[1,0]
	v_mov_b32_e32 v18, v167
	v_rcp_f32_e32 v16, v16
	v_rcp_f32_e32 v17, v17
	v_mov_b32_e32 v19, v167
	v_cvt_pk_fp8_f32 v18, v6, v7
	v_cvt_pk_fp8_f32 v19, v12, v13
	v_med3_f32 v15, v15, s65, v179
	v_pk_fma_f32 v[6:7], v[14:15], v[10:11], v[10:11]
	v_cvt_pk_fp8_f32 v18, v4, v5 op_sel:[0,0,1]
	v_pk_mul_f32 v[6:7], v[6:7], v[16:17]
	global_store_dwordx2 v[2:3], v[148:149], off
	v_cvt_pk_fp8_f32 v19, v6, v7 op_sel:[0,0,1]
	v_add_co_u32_e32 v2, vcc, 0x58000, v2
	s_mov_b64 s[44:45], -1
	s_nop 0
	v_addc_co_u32_e32 v3, vcc, 0, v3, vcc
	s_and_b64 vcc, s[42:43], exec
	global_store_dwordx2 v[2:3], v[18:19], off
	s_cbranch_vccz .LBB0_1434
	s_ashr_i32 s41, s40, 31
	s_lshl_b64 s[42:43], s[40:41], 14
	s_add_u32 s41, s88, s42
	s_addc_u32 s44, s89, s43
	s_lshl_b32 s42, s38, 7
	s_ashr_i32 s43, s42, 31
	s_lshl_b64 s[42:43], s[42:43], 2
	s_add_u32 s41, s41, s42
	s_addc_u32 s43, s44, s43
	s_lshl_b32 s39, s39, 2
	s_add_u32 s42, s41, s39
	s_addc_u32 s43, s43, 0
	v_lshlrev_b32_e32 v166, 2, v8
	v_lshl_add_u64 v[2:3], s[42:43], 0, v[166:167]
	v_lshl_add_u64 v[4:5], v[2:3], 0, 16
	s_mov_b64 s[44:45], 0
	global_load_dwordx4 v[30:33], v[2:3], off
	global_load_dwordx4 v[22:25], v[4:5], off
	v_lshl_add_u64 v[4:5], v[2:3], 0, s[12:13]
	global_load_dwordx4 v[26:29], v[4:5], off
	v_lshl_add_u64 v[2:3], v[2:3], 0, s[14:15]
	global_load_dwordx4 v[18:21], v[2:3], off
	s_branch .LBB0_1434

.LBB0_1547:
	ds_read_b128 v[10:13], v183
	ds_read_b128 v[14:17], v183 offset:1024
	ds_read_b128 v[174:177], v183 offset:2048
	ds_read_b128 v[178:181], v183 offset:3072
	s_add_u32 s46, s44, 0xfffc0080
	s_addc_u32 s47, s45, -1
	s_cmp_eq_u32 s80, 12
	s_cselect_b32 s49, s27, s47
	s_cselect_b32 s48, s31, s46
	s_cselect_b32 s47, s25, s79
	s_cselect_b32 s46, s39, s78
	s_mov_b32 m0, s68
	v_lshl_add_u64 v[2:3], s[44:45], 0, v[170:171]
	ds_read_b128 v[188:191], v184
	ds_read_b128 v[192:195], v184 offset:1024
	ds_read_b128 v[196:199], v184 offset:2048
	ds_read_b128 v[200:203], v184 offset:3072
	ds_read_b128 v[204:207], v184 offset:4096
	ds_read_b128 v[208:211], v184 offset:5120
	ds_read_b128 v[212:215], v184 offset:6144
	ds_read_b128 v[216:219], v184 offset:7168
	global_load_lds_dwordx4 v[2:3], off
	v_lshl_add_u64 v[2:3], s[44:45], 0, v[172:173]
	s_mov_b32 m0, s69
	s_nop 0
	global_load_lds_dwordx4 v[2:3], off
	ds_read_b128 v[220:223], v185
	ds_read_b128 v[224:227], v185 offset:1024
	ds_read_b128 v[228:231], v185 offset:2048
	ds_read_b128 v[232:235], v185 offset:3072
	s_waitcnt vmcnt(8) lgkmcnt(0)
	s_barrier
	v_mfma_f32_16x16x128_f8f6f4 v[150:153], v[10:17], v[188:195], v[150:153]
	v_mfma_f32_16x16x128_f8f6f4 v[146:149], v[174:181], v[188:195], v[146:149]
	v_mfma_f32_16x16x128_f8f6f4 v[134:137], v[10:17], v[196:203], v[134:137]
	v_mfma_f32_16x16x128_f8f6f4 v[130:133], v[174:181], v[196:203], v[130:133]
	v_mfma_f32_16x16x128_f8f6f4 v[118:121], v[10:17], v[204:211], v[118:121]
	v_mfma_f32_16x16x128_f8f6f4 v[114:117], v[174:181], v[204:211], v[114:117]
	v_mfma_f32_16x16x128_f8f6f4 v[86:89], v[10:17], v[212:219], v[86:89]
	v_mfma_f32_16x16x128_f8f6f4 v[82:85], v[174:181], v[212:219], v[82:85]
	v_mfma_f32_16x16x128_f8f6f4 v[158:161], v[220:227], v[188:195], v[158:161]
	v_mfma_f32_16x16x128_f8f6f4 v[154:157], v[228:235], v[188:195], v[154:157]
	v_mfma_f32_16x16x128_f8f6f4 v[142:145], v[220:227], v[196:203], v[142:145]
	v_mfma_f32_16x16x128_f8f6f4 v[138:141], v[228:235], v[196:203], v[138:141]
	v_mfma_f32_16x16x128_f8f6f4 v[126:129], v[220:227], v[204:211], v[126:129]
	v_mfma_f32_16x16x128_f8f6f4 v[122:125], v[228:235], v[204:211], v[122:125]
	v_mfma_f32_16x16x128_f8f6f4 v[94:97], v[220:227], v[212:219], v[94:97]
	v_mfma_f32_16x16x128_f8f6f4 v[90:93], v[228:235], v[212:219], v[90:93]
	s_barrier
	ds_read_b128 v[188:191], v184 offset:16384
	ds_read_b128 v[192:195], v184 offset:17408
	ds_read_b128 v[196:199], v184 offset:18432
	ds_read_b128 v[200:203], v184 offset:19456
	ds_read_b128 v[204:207], v184 offset:20480
	ds_read_b128 v[208:211], v184 offset:21504
	ds_read_b128 v[212:215], v184 offset:22528
	ds_read_b128 v[216:219], v184 offset:23552
	s_mov_b32 m0, s70
	v_lshl_add_u64 v[6:7], s[46:47], 0, v[164:165]
	global_load_lds_dwordx4 v[6:7], off
	v_lshl_add_u64 v[8:9], s[46:47], 0, v[168:169]
	s_mov_b32 m0, s71
	s_nop 0
	global_load_lds_dwordx4 v[8:9], off
	s_mov_b32 m0, s54
	v_lshl_add_u64 v[2:3], s[48:49], 0, v[162:163]
	global_load_lds_dwordx4 v[2:3], off
	v_lshl_add_u64 v[4:5], s[48:49], 0, v[166:167]
	s_mov_b32 m0, s55
	s_nop 0
	global_load_lds_dwordx4 v[4:5], off
	s_add_u32 s82, s46, 0x40000
	s_addc_u32 s83, s47, 0
	s_mov_b32 m0, s72
	v_lshl_add_u64 v[236:237], s[82:83], 0, v[164:165]
	global_load_lds_dwordx4 v[236:237], off
	v_lshl_add_u64 v[236:237], s[82:83], 0, v[168:169]
	s_mov_b32 m0, s73
	s_nop 0
	global_load_lds_dwordx4 v[236:237], off
	s_waitcnt vmcnt(8) lgkmcnt(0)
	s_barrier
	v_mfma_f32_16x16x128_f8f6f4 v[110:113], v[10:17], v[188:195], v[110:113]
	v_mfma_f32_16x16x128_f8f6f4 v[102:105], v[174:181], v[188:195], v[102:105]
	v_mfma_f32_16x16x128_f8f6f4 v[78:81], v[10:17], v[196:203], v[78:81]
	v_mfma_f32_16x16x128_f8f6f4 v[70:73], v[174:181], v[196:203], v[70:73]
	v_mfma_f32_16x16x128_f8f6f4 v[62:65], v[10:17], v[204:211], v[62:65]
	v_mfma_f32_16x16x128_f8f6f4 v[54:57], v[174:181], v[204:211], v[54:57]
	v_mfma_f32_16x16x128_f8f6f4 v[46:49], v[10:17], v[212:219], v[46:49]
	v_mfma_f32_16x16x128_f8f6f4 v[42:45], v[174:181], v[212:219], v[42:45]
	v_mfma_f32_16x16x128_f8f6f4 v[106:109], v[220:227], v[188:195], v[106:109]
	v_mfma_f32_16x16x128_f8f6f4 v[98:101], v[228:235], v[188:195], v[98:101]
	v_mfma_f32_16x16x128_f8f6f4 v[74:77], v[220:227], v[196:203], v[74:77]
	v_mfma_f32_16x16x128_f8f6f4 v[66:69], v[228:235], v[196:203], v[66:69]
	v_mfma_f32_16x16x128_f8f6f4 v[58:61], v[220:227], v[204:211], v[58:61]
	v_mfma_f32_16x16x128_f8f6f4 v[50:53], v[228:235], v[204:211], v[50:53]
	v_mfma_f32_16x16x128_f8f6f4 v[38:41], v[220:227], v[212:219], v[38:41]
	v_mfma_f32_16x16x128_f8f6f4 v[34:37], v[228:235], v[212:219], v[34:37]
	s_barrier
	ds_read_b128 v[10:13], v186
	ds_read_b128 v[14:17], v186 offset:1024
	ds_read_b128 v[174:177], v186 offset:2048
	ds_read_b128 v[178:181], v186 offset:3072
	s_add_u32 s48, s48, 0x40000
	s_addc_u32 s49, s49, 0
	s_mov_b32 m0, s56
	v_lshl_add_u64 v[220:221], s[48:49], 0, v[162:163]
	ds_read_b128 v[188:191], v184 offset:32768
	ds_read_b128 v[192:195], v184 offset:33792
	ds_read_b128 v[196:199], v184 offset:34816
	ds_read_b128 v[200:203], v184 offset:35840
	ds_read_b128 v[204:207], v184 offset:36864
	ds_read_b128 v[208:211], v184 offset:37888
	ds_read_b128 v[212:215], v184 offset:38912
	ds_read_b128 v[216:219], v184 offset:39936
	global_load_lds_dwordx4 v[220:221], off
	v_lshl_add_u64 v[220:221], s[48:49], 0, v[166:167]
	s_mov_b32 m0, s57
	s_nop 0
	global_load_lds_dwordx4 v[220:221], off
	ds_read_b128 v[220:223], v187
	ds_read_b128 v[224:227], v187 offset:1024
	ds_read_b128 v[228:231], v187 offset:2048
	ds_read_b128 v[232:235], v187 offset:3072
	s_waitcnt vmcnt(8) lgkmcnt(0)
	s_barrier
	v_mfma_f32_16x16x128_f8f6f4 v[150:153], v[10:17], v[188:195], v[150:153]
	v_mfma_f32_16x16x128_f8f6f4 v[146:149], v[174:181], v[188:195], v[146:149]
	v_mfma_f32_16x16x128_f8f6f4 v[134:137], v[10:17], v[196:203], v[134:137]
	v_mfma_f32_16x16x128_f8f6f4 v[130:133], v[174:181], v[196:203], v[130:133]
	v_mfma_f32_16x16x128_f8f6f4 v[118:121], v[10:17], v[204:211], v[118:121]
	v_mfma_f32_16x16x128_f8f6f4 v[114:117], v[174:181], v[204:211], v[114:117]
	v_mfma_f32_16x16x128_f8f6f4 v[86:89], v[10:17], v[212:219], v[86:89]
	v_mfma_f32_16x16x128_f8f6f4 v[82:85], v[174:181], v[212:219], v[82:85]
	v_mfma_f32_16x16x128_f8f6f4 v[158:161], v[220:227], v[188:195], v[158:161]
	v_mfma_f32_16x16x128_f8f6f4 v[154:157], v[228:235], v[188:195], v[154:157]
	v_mfma_f32_16x16x128_f8f6f4 v[142:145], v[220:227], v[196:203], v[142:145]
	v_mfma_f32_16x16x128_f8f6f4 v[138:141], v[228:235], v[196:203], v[138:141]
	v_mfma_f32_16x16x128_f8f6f4 v[126:129], v[220:227], v[204:211], v[126:129]
	v_mfma_f32_16x16x128_f8f6f4 v[122:125], v[228:235], v[204:211], v[122:125]
	v_mfma_f32_16x16x128_f8f6f4 v[94:97], v[220:227], v[212:219], v[94:97]
	v_mfma_f32_16x16x128_f8f6f4 v[90:93], v[228:235], v[212:219], v[90:93]
	s_barrier
	ds_read_b128 v[188:191], v184 offset:49152
	ds_read_b128 v[192:195], v184 offset:50176
	ds_read_b128 v[196:199], v184 offset:51200
	ds_read_b128 v[200:203], v184 offset:52224
	ds_read_b128 v[204:207], v184 offset:53248
	ds_read_b128 v[208:211], v184 offset:54272
	ds_read_b128 v[212:215], v184 offset:55296
	ds_read_b128 v[216:219], v184 offset:56320
	s_mov_b32 m0, s74
	v_lshl_add_u64 v[6:7], v[6:7], 0, s[10:11]
	global_load_lds_dwordx4 v[6:7], off
	v_lshl_add_u64 v[6:7], v[8:9], 0, s[10:11]
	s_mov_b32 m0, s75
	s_nop 0
	global_load_lds_dwordx4 v[6:7], off
	s_mov_b32 m0, s59
	v_lshl_add_u64 v[2:3], v[2:3], 0, s[10:11]
	global_load_lds_dwordx4 v[2:3], off
	v_lshl_add_u64 v[2:3], v[4:5], 0, s[10:11]
	s_mov_b32 m0, s60
	s_nop 0
	global_load_lds_dwordx4 v[2:3], off
	s_add_u32 s46, s46, 0x40080
	s_addc_u32 s47, s47, 0
	s_mov_b32 m0, s76
	v_lshl_add_u64 v[2:3], s[46:47], 0, v[164:165]
	global_load_lds_dwordx4 v[2:3], off
	v_lshl_add_u64 v[2:3], s[46:47], 0, v[168:169]
	s_mov_b32 m0, s77
	s_nop 0
	global_load_lds_dwordx4 v[2:3], off
	s_waitcnt vmcnt(8) lgkmcnt(0)
	s_barrier
	v_mfma_f32_16x16x128_f8f6f4 v[110:113], v[10:17], v[188:195], v[110:113]
	v_mfma_f32_16x16x128_f8f6f4 v[102:105], v[174:181], v[188:195], v[102:105]
	v_mfma_f32_16x16x128_f8f6f4 v[78:81], v[10:17], v[196:203], v[78:81]
	v_mfma_f32_16x16x128_f8f6f4 v[70:73], v[174:181], v[196:203], v[70:73]
	v_mfma_f32_16x16x128_f8f6f4 v[62:65], v[10:17], v[204:211], v[62:65]
	v_mfma_f32_16x16x128_f8f6f4 v[54:57], v[174:181], v[204:211], v[54:57]
	v_mfma_f32_16x16x128_f8f6f4 v[46:49], v[10:17], v[212:219], v[46:49]
	v_mfma_f32_16x16x128_f8f6f4 v[42:45], v[174:181], v[212:219], v[42:45]
	v_mfma_f32_16x16x128_f8f6f4 v[106:109], v[220:227], v[188:195], v[106:109]
	v_mfma_f32_16x16x128_f8f6f4 v[98:101], v[228:235], v[188:195], v[98:101]
	v_mfma_f32_16x16x128_f8f6f4 v[74:77], v[220:227], v[196:203], v[74:77]
	v_mfma_f32_16x16x128_f8f6f4 v[66:69], v[228:235], v[196:203], v[66:69]
	v_mfma_f32_16x16x128_f8f6f4 v[58:61], v[220:227], v[204:211], v[58:61]
	v_mfma_f32_16x16x128_f8f6f4 v[50:53], v[228:235], v[204:211], v[50:53]
	v_mfma_f32_16x16x128_f8f6f4 v[38:41], v[220:227], v[212:219], v[38:41]
	v_mfma_f32_16x16x128_f8f6f4 v[34:37], v[228:235], v[212:219], v[34:37]
	s_add_i32 s80, s80, 2
	s_add_u32 s44, s44, 0x100
	s_addc_u32 s45, s45, 0
	s_add_u32 s78, s78, 0x100
	s_addc_u32 s79, s79, 0
	s_cmp_gt_u32 s80, 13
	s_barrier
	s_cbranch_scc0 .LBB0_1547
	v_mov_b32_e32 v2, v0
	s_nop 15
	s_nop 15
	s_lshl_b32 s27, s40, 8
	v_readfirstlane_b32 s25, v2
	s_ashr_i32 s31, s25, 2
	s_andn2_b32 s31, s31, 63
	s_add_i32 s31, s31, s27
	s_lshr_b32 s25, s25, 1
	v_and_or_b32 v10, v2, 15, s31
	s_and_b32 s25, s25, 0x60
	v_lshrrev_b32_e32 v2, 1, v2
	s_lshl_b32 s27, s38, 8
	v_and_b32_e32 v4, 24, v2
	s_or_b32 s27, s25, s27
	v_or_b32_e32 v2, s27, v4
	v_ashrrev_i32_e32 v11, 31, v10
	v_ashrrev_i32_e32 v3, 31, v2
	v_lshlrev_b64 v[6:7], 12, v[10:11]
	v_lshl_add_u64 v[6:7], s[8:9], 0, v[6:7]
	v_lshlrev_b64 v[12:13], 1, v[2:3]
	s_waitcnt vmcnt(6)
	v_lshl_add_u64 v[2:3], v[6:7], 0, v[12:13]
	v_pk_fma_f32 v[6:7], v[150:151], s[18:19], v[22:23] op_sel_hi:[1,0,1]
	v_pk_fma_f32 v[8:9], v[152:153], s[18:19], v[24:25] op_sel_hi:[1,0,1]
	v_cvt_pk_bf16_f32 v6, v6, v7
	v_pk_fma_f32 v[14:15], v[148:149], s[18:19], v[20:21] op_sel_hi:[1,0,1]
	v_cvt_pk_bf16_f32 v7, v8, v9
	v_pk_fma_f32 v[16:17], v[146:147], s[18:19], v[18:19] op_sel_hi:[1,0,1]
	v_pk_fma_f32 v[130:131], v[130:131], s[18:19], v[18:19] op_sel_hi:[1,0,1]
	v_cvt_pk_bf16_f32 v8, v16, v17
	v_cvt_pk_bf16_f32 v9, v14, v15
	global_store_dwordx4 v[2:3], v[6:9], off
	v_pk_fma_f32 v[14:15], v[156:157], s[18:19], v[28:29] op_sel_hi:[1,0,1]
	v_pk_fma_f32 v[16:17], v[154:155], s[18:19], v[26:27] op_sel_hi:[1,0,1]
	v_pk_fma_f32 v[6:7], v[158:159], s[18:19], v[30:31] op_sel_hi:[1,0,1]
	v_pk_fma_f32 v[8:9], v[160:161], s[18:19], v[32:33] op_sel_hi:[1,0,1]
	v_cvt_pk_bf16_f32 v6, v6, v7
	v_pk_fma_f32 v[114:115], v[114:115], s[18:19], v[18:19] op_sel_hi:[1,0,1]
	v_cvt_pk_bf16_f32 v7, v8, v9
	v_cvt_pk_bf16_f32 v8, v16, v17
	v_cvt_pk_bf16_f32 v9, v14, v15
	global_store_dwordx4 v[2:3], v[6:9], off offset:256
	v_pk_fma_f32 v[16:17], v[132:133], s[18:19], v[20:21] op_sel_hi:[1,0,1]
	s_mov_b32 s27, 0x80000
	v_or_b32_e32 v6, 16, v10
	v_ashrrev_i32_e32 v7, 31, v6
	v_lshlrev_b64 v[6:7], 12, v[6:7]
	v_lshl_add_u64 v[6:7], s[8:9], 0, v[6:7]
	v_lshl_add_u64 v[14:15], v[6:7], 0, v[12:13]
	v_pk_fma_f32 v[6:7], v[134:135], s[18:19], v[22:23] op_sel_hi:[1,0,1]
	v_pk_fma_f32 v[8:9], v[136:137], s[18:19], v[24:25] op_sel_hi:[1,0,1]
	v_cvt_pk_bf16_f32 v6, v6, v7
	s_mov_b64 s[38:39], 0x80000
	v_cvt_pk_bf16_f32 v7, v8, v9
	v_cvt_pk_bf16_f32 v8, v130, v131
	v_cvt_pk_bf16_f32 v9, v16, v17
	global_store_dwordx4 v[14:15], v[6:9], off
	v_pk_fma_f32 v[16:17], v[140:141], s[18:19], v[28:29] op_sel_hi:[1,0,1]
	v_pk_fma_f32 v[130:131], v[138:139], s[18:19], v[26:27] op_sel_hi:[1,0,1]
	v_pk_fma_f32 v[6:7], v[142:143], s[18:19], v[30:31] op_sel_hi:[1,0,1]
	v_pk_fma_f32 v[8:9], v[144:145], s[18:19], v[32:33] op_sel_hi:[1,0,1]
	v_cvt_pk_bf16_f32 v6, v6, v7
	v_readlane_b32 s68, v254, 0
	v_cvt_pk_bf16_f32 v7, v8, v9
	v_cvt_pk_bf16_f32 v8, v130, v131
	v_cvt_pk_bf16_f32 v9, v16, v17
	global_store_dwordx4 v[14:15], v[6:9], off offset:256
	v_pk_fma_f32 v[16:17], v[116:117], s[18:19], v[20:21] op_sel_hi:[1,0,1]
	v_readlane_b32 s69, v254, 1
	v_or_b32_e32 v6, 32, v10
	v_ashrrev_i32_e32 v7, 31, v6
	v_lshlrev_b64 v[6:7], 12, v[6:7]
	v_lshl_add_u64 v[6:7], s[8:9], 0, v[6:7]
	v_lshl_add_u64 v[14:15], v[6:7], 0, v[12:13]
	v_pk_fma_f32 v[6:7], v[118:119], s[18:19], v[22:23] op_sel_hi:[1,0,1]
	v_pk_fma_f32 v[8:9], v[120:121], s[18:19], v[24:25] op_sel_hi:[1,0,1]
	v_cvt_pk_bf16_f32 v6, v6, v7
	v_readlane_b32 s70, v254, 2
	v_cvt_pk_bf16_f32 v7, v8, v9
	v_cvt_pk_bf16_f32 v8, v114, v115
	v_cvt_pk_bf16_f32 v9, v16, v17
	global_store_dwordx4 v[14:15], v[6:9], off
	v_pk_fma_f32 v[16:17], v[124:125], s[18:19], v[28:29] op_sel_hi:[1,0,1]
	v_pk_fma_f32 v[114:115], v[122:123], s[18:19], v[26:27] op_sel_hi:[1,0,1]
	v_pk_fma_f32 v[6:7], v[126:127], s[18:19], v[30:31] op_sel_hi:[1,0,1]
	v_pk_fma_f32 v[8:9], v[128:129], s[18:19], v[32:33] op_sel_hi:[1,0,1]
	v_cvt_pk_bf16_f32 v6, v6, v7
	v_readlane_b32 s71, v254, 3
	v_cvt_pk_bf16_f32 v7, v8, v9
	v_cvt_pk_bf16_f32 v8, v114, v115
	v_cvt_pk_bf16_f32 v9, v16, v17
	global_store_dwordx4 v[14:15], v[6:9], off offset:256
	v_pk_fma_f32 v[14:15], v[82:83], s[18:19], v[18:19] op_sel_hi:[1,0,1]
	v_readlane_b32 s72, v254, 4
	v_or_b32_e32 v6, 48, v10
	v_ashrrev_i32_e32 v7, 31, v6
	v_lshlrev_b64 v[6:7], 12, v[6:7]
	v_lshl_add_u64 v[6:7], s[8:9], 0, v[6:7]
	v_lshl_add_u64 v[10:11], v[6:7], 0, v[12:13]
	v_pk_fma_f32 v[8:9], v[88:89], s[18:19], v[24:25] op_sel_hi:[1,0,1]
	v_pk_fma_f32 v[6:7], v[86:87], s[18:19], v[22:23] op_sel_hi:[1,0,1]
	v_pk_fma_f32 v[12:13], v[84:85], s[18:19], v[20:21] op_sel_hi:[1,0,1]
	v_cvt_pk_bf16_f32 v6, v6, v7
	v_cvt_pk_bf16_f32 v7, v8, v9
	v_cvt_pk_bf16_f32 v8, v14, v15
	v_pk_fma_f32 v[14:15], v[90:91], s[18:19], v[26:27] op_sel_hi:[1,0,1]
	v_cvt_pk_bf16_f32 v9, v12, v13
	global_store_dwordx4 v[10:11], v[6:9], off
	v_pk_fma_f32 v[12:13], v[92:93], s[18:19], v[28:29] op_sel_hi:[1,0,1]
	v_readlane_b32 s73, v254, 5
	v_pk_fma_f32 v[8:9], v[96:97], s[18:19], v[32:33] op_sel_hi:[1,0,1]
	v_pk_fma_f32 v[6:7], v[94:95], s[18:19], v[30:31] op_sel_hi:[1,0,1]
	v_readlane_b32 s74, v254, 6
	v_cvt_pk_bf16_f32 v6, v6, v7
	v_cvt_pk_bf16_f32 v7, v8, v9
	v_cvt_pk_bf16_f32 v8, v14, v15
	v_cvt_pk_bf16_f32 v9, v12, v13
	global_store_dwordx4 v[10:11], v[6:9], off offset:256
	v_pk_fma_f32 v[12:13], v[104:105], s[18:19], v[20:21] op_sel_hi:[1,0,1]
	v_pk_fma_f32 v[14:15], v[102:103], s[18:19], v[18:19] op_sel_hi:[1,0,1]
	v_pk_fma_f32 v[8:9], v[112:113], s[18:19], v[24:25] op_sel_hi:[1,0,1]
	v_pk_fma_f32 v[6:7], v[110:111], s[18:19], v[22:23] op_sel_hi:[1,0,1]
	v_lshl_add_u64 v[10:11], v[2:3], 0, s[38:39]
	v_cvt_pk_bf16_f32 v6, v6, v7
	v_cvt_pk_bf16_f32 v7, v8, v9
	v_cvt_pk_bf16_f32 v8, v14, v15
	v_cvt_pk_bf16_f32 v9, v12, v13
	v_add_co_u32_e32 v12, vcc, s27, v2
	v_pk_fma_f32 v[14:15], v[98:99], s[18:19], v[26:27] op_sel_hi:[1,0,1]
	s_nop 0
	v_addc_co_u32_e32 v13, vcc, 0, v3, vcc
	global_store_dwordx4 v[12:13], v[6:9], off
	v_pk_fma_f32 v[12:13], v[100:101], s[18:19], v[28:29] op_sel_hi:[1,0,1]
	s_mov_b32 s27, 0x90000
	v_pk_fma_f32 v[8:9], v[108:109], s[18:19], v[32:33] op_sel_hi:[1,0,1]
	v_pk_fma_f32 v[6:7], v[106:107], s[18:19], v[30:31] op_sel_hi:[1,0,1]
	s_mov_b64 s[38:39], 0x90000
	v_cvt_pk_bf16_f32 v6, v6, v7
	v_cvt_pk_bf16_f32 v7, v8, v9
	v_cvt_pk_bf16_f32 v8, v14, v15
	v_cvt_pk_bf16_f32 v9, v12, v13
	global_store_dwordx4 v[10:11], v[6:9], off offset:256
	v_pk_fma_f32 v[12:13], v[72:73], s[18:19], v[20:21] op_sel_hi:[1,0,1]
	v_pk_fma_f32 v[14:15], v[70:71], s[18:19], v[18:19] op_sel_hi:[1,0,1]
	v_pk_fma_f32 v[8:9], v[80:81], s[18:19], v[24:25] op_sel_hi:[1,0,1]
	v_pk_fma_f32 v[6:7], v[78:79], s[18:19], v[22:23] op_sel_hi:[1,0,1]
	v_lshl_add_u64 v[10:11], v[2:3], 0, s[38:39]
	v_cvt_pk_bf16_f32 v6, v6, v7
	v_cvt_pk_bf16_f32 v7, v8, v9
	v_cvt_pk_bf16_f32 v8, v14, v15
	v_cvt_pk_bf16_f32 v9, v12, v13
	v_add_co_u32_e32 v12, vcc, s27, v2
	v_pk_fma_f32 v[14:15], v[66:67], s[18:19], v[26:27] op_sel_hi:[1,0,1]
	s_nop 0
	v_addc_co_u32_e32 v13, vcc, 0, v3, vcc
	global_store_dwordx4 v[12:13], v[6:9], off
	v_pk_fma_f32 v[12:13], v[68:69], s[18:19], v[28:29] op_sel_hi:[1,0,1]
	s_mov_b64 s[38:39], 0xa0000
	v_pk_fma_f32 v[8:9], v[76:77], s[18:19], v[32:33] op_sel_hi:[1,0,1]
	v_pk_fma_f32 v[6:7], v[74:75], s[18:19], v[30:31] op_sel_hi:[1,0,1]
	v_readlane_b32 s75, v254, 7
	v_cvt_pk_bf16_f32 v6, v6, v7
	v_cvt_pk_bf16_f32 v7, v8, v9
	v_cvt_pk_bf16_f32 v8, v14, v15
	v_cvt_pk_bf16_f32 v9, v12, v13
	global_store_dwordx4 v[10:11], v[6:9], off offset:256
	v_pk_fma_f32 v[12:13], v[56:57], s[18:19], v[20:21] op_sel_hi:[1,0,1]
	v_pk_fma_f32 v[14:15], v[54:55], s[18:19], v[18:19] op_sel_hi:[1,0,1]
	v_pk_fma_f32 v[8:9], v[64:65], s[18:19], v[24:25] op_sel_hi:[1,0,1]
	v_pk_fma_f32 v[6:7], v[62:63], s[18:19], v[22:23] op_sel_hi:[1,0,1]
	v_lshl_add_u64 v[10:11], v[2:3], 0, s[38:39]
	v_cvt_pk_bf16_f32 v6, v6, v7
	v_cvt_pk_bf16_f32 v7, v8, v9
	v_cvt_pk_bf16_f32 v8, v14, v15
	v_cvt_pk_bf16_f32 v9, v12, v13
	v_add_co_u32_e32 v12, vcc, s66, v2
	v_pk_fma_f32 v[14:15], v[50:51], s[18:19], v[26:27] op_sel_hi:[1,0,1]
	s_nop 0
	v_addc_co_u32_e32 v13, vcc, 0, v3, vcc
	global_store_dwordx4 v[12:13], v[6:9], off
	v_pk_fma_f32 v[12:13], v[52:53], s[18:19], v[28:29] op_sel_hi:[1,0,1]
	s_mov_b64 s[38:39], -1
	v_pk_fma_f32 v[8:9], v[60:61], s[18:19], v[32:33] op_sel_hi:[1,0,1]
	v_pk_fma_f32 v[6:7], v[58:59], s[18:19], v[30:31] op_sel_hi:[1,0,1]
	s_nop 0
	v_cvt_pk_bf16_f32 v6, v6, v7
	v_cvt_pk_bf16_f32 v7, v8, v9
	v_cvt_pk_bf16_f32 v8, v14, v15
	v_cvt_pk_bf16_f32 v9, v12, v13
	global_store_dwordx4 v[10:11], v[6:9], off offset:256
	v_lshl_add_u64 v[10:11], v[2:3], 0, s[20:21]
	v_add_co_u32_e32 v2, vcc, s67, v2
	v_pk_fma_f32 v[8:9], v[48:49], s[18:19], v[24:25] op_sel_hi:[1,0,1]
	v_pk_fma_f32 v[6:7], v[46:47], s[18:19], v[22:23] op_sel_hi:[1,0,1]
	v_pk_fma_f32 v[12:13], v[44:45], s[18:19], v[20:21] op_sel_hi:[1,0,1]
	v_pk_fma_f32 v[14:15], v[42:43], s[18:19], v[18:19] op_sel_hi:[1,0,1]
	v_cvt_pk_bf16_f32 v6, v6, v7
	v_cvt_pk_bf16_f32 v7, v8, v9
	v_addc_co_u32_e32 v3, vcc, 0, v3, vcc
	v_cvt_pk_bf16_f32 v8, v14, v15
	v_cvt_pk_bf16_f32 v9, v12, v13
	global_store_dwordx4 v[2:3], v[6:9], off
	s_and_b64 vcc, s[42:43], exec
	v_pk_fma_f32 v[2:3], v[40:41], s[18:19], v[32:33] op_sel_hi:[1,0,1]
	v_pk_fma_f32 v[6:7], v[38:39], s[18:19], v[30:31] op_sel_hi:[1,0,1]
	v_pk_fma_f32 v[8:9], v[34:35], s[18:19], v[26:27] op_sel_hi:[1,0,1]
	v_pk_fma_f32 v[12:13], v[36:37], s[18:19], v[28:29] op_sel_hi:[1,0,1]
	v_cvt_pk_bf16_f32 v6, v6, v7
	v_cvt_pk_bf16_f32 v7, v2, v3
	v_cvt_pk_bf16_f32 v8, v8, v9
	s_nop 0
	v_cvt_pk_bf16_f32 v9, v12, v13
	global_store_dwordx4 v[10:11], v[6:9], off offset:256
	s_cbranch_vccz .LBB0_1541
	s_lshl_b32 s27, s24, 8
	s_or_b32 s25, s25, s27
	v_or_b32_e32 v2, s25, v4
	v_ashrrev_i32_e32 v3, 31, v2
	v_mov_b32_e32 v18, 0
	s_and_b64 vcc, exec, s[6:7]
	v_mov_b32_e32 v22, 0
	v_mov_b32_e32 v23, 0
	v_mov_b32_e32 v24, 0
	v_mov_b32_e32 v25, 0
	s_cbranch_vccnz .LBB0_1551
	s_ashr_i32 s27, s26, 31
	s_lshl_b64 s[38:39], s[26:27], 13
	s_add_u32 s38, s68, s38
	s_addc_u32 s39, s69, s39
	v_lshl_add_u64 v[4:5], v[2:3], 2, s[38:39]
	global_load_dwordx4 v[22:25], v[4:5], off
